# peer_gather epilogue: next-norm gain kept in VGPRs, residual row prefetched at token prologue
# speedup vs baseline: 1.0150x; 1.0001x over previous
.LBB0_759:
	s_or_b64 exec, exec, s[6:7]
	v_readlane_b32 s8, v255, 42
	v_readlane_b32 s9, v255, 43
	s_mov_b64 s[6:7], -1
	s_and_b64 vcc, exec, s[8:9]
	s_waitcnt lgkmcnt(0)
	s_barrier
	s_cbranch_vccz .LBB0_766
	v_readlane_b32 s10, v253, 0
	v_readlane_b32 s11, v253, 1
	v_mov_b32_e32 v3, v175
	v_readlane_b32 s6, v253, 8
	v_ashrrev_i32_e32 v0, 6, v3
	s_nop 0
	v_add_u32_e32 v0, s6, v0
	v_cmp_gt_i32_e32 vcc, s87, v0
	s_and_saveexec_b64 s[6:7], vcc
	s_mov_b32 s18, 0x800000
	s_cbranch_execz .LBB0_765
	v_ashrrev_i32_e32 v1, 31, v0
	v_and_b32_e32 v2, 15, v3
	v_lshlrev_b64 v[34:35], 9, v[0:1]
	v_lshl_add_u64 v[4:5], s[94:95], 0, v[34:35]
	v_lshlrev_b32_e32 v144, 2, v2
	v_lshl_add_u64 v[4:5], v[4:5], 0, v[144:145]
	global_load_dword v92, v[4:5], off
	v_readlane_b32 s12, v255, 7
	v_readlane_b32 s13, v255, 8
	s_lshl_b64 s[8:9], s[12:13], 17
	s_add_u32 s8, s88, s8
	s_addc_u32 s9, s89, s9
	s_lshl_b64 s[14:15], s[12:13], 23
	v_readlane_b32 s12, v253, 29
	v_readlane_b32 s13, v253, 30
	s_add_u32 s12, s12, s14
	v_and_b32_e32 v28, 63, v3
	s_addc_u32 s13, s13, s15
	v_readlane_b32 s16, v253, 27
	v_lshlrev_b32_e32 v144, 3, v28
	v_readlane_b32 s17, v253, 28
	s_add_u32 s14, s16, s14
	v_lshl_add_u64 v[6:7], s[12:13], 0, v[144:145]
	s_addc_u32 s15, s17, s15
	v_lshl_add_u64 v[4:5], s[14:15], 0, v[144:145]
	s_load_dwordx2 s[10:11], s[10:11], 0xf0
	v_lshlrev_b32_e32 v144, 5, v28
	v_and_b32_e32 v1, 32, v3
	v_cmp_eq_u32_e64 s[40:41], 0, v1
	v_and_b32_e32 v1, 16, v3
	v_and_b32_e32 v93, 60, v3
	v_cmp_eq_u32_e64 s[42:43], 0, v1
	v_and_b32_e32 v1, 8, v3
	v_cmp_eq_u32_e64 s[44:45], 0, v1
	v_and_b32_e32 v1, 4, v3
	v_or_b32_e32 v34, v34, v93
	v_cmp_eq_u32_e64 s[46:47], 0, v1
	s_waitcnt vmcnt(0)
	v_readlane_b32 s12, v92, 0
	s_ashr_i32 s13, s12, 31
	s_lshl_b64 s[12:13], s[12:13], 9
	v_lshl_add_u64 v[8:9], v[4:5], 0, s[12:13]
	v_lshl_add_u64 v[10:11], v[6:7], 0, s[12:13]
	v_readlane_b32 s12, v92, 1
	s_ashr_i32 s13, s12, 31
	s_lshl_b64 s[12:13], s[12:13], 9
	v_lshl_add_u64 v[12:13], v[6:7], 0, s[12:13]
	global_load_dwordx2 v[8:9], v[8:9], off
	s_nop 0
	global_load_dwordx2 v[82:83], v[10:11], off
	global_load_dwordx2 v[80:81], v[12:13], off
	v_lshl_add_u64 v[10:11], v[4:5], 0, s[12:13]
	v_readlane_b32 s12, v92, 2
	s_ashr_i32 s13, s12, 31
	s_lshl_b64 s[12:13], s[12:13], 9
	v_lshl_add_u64 v[12:13], v[4:5], 0, s[12:13]
	v_lshl_add_u64 v[14:15], v[6:7], 0, s[12:13]
	v_readlane_b32 s12, v92, 3
	s_ashr_i32 s13, s12, 31
	s_lshl_b64 s[12:13], s[12:13], 9
	v_lshl_add_u64 v[16:17], v[6:7], 0, s[12:13]
	global_load_dwordx2 v[10:11], v[10:11], off
	s_nop 0
	global_load_dwordx2 v[12:13], v[12:13], off
	s_nop 0
	global_load_dwordx2 v[78:79], v[14:15], off
	global_load_dwordx2 v[76:77], v[16:17], off
	v_lshl_add_u64 v[14:15], v[4:5], 0, s[12:13]
	v_readlane_b32 s12, v92, 4
	s_ashr_i32 s13, s12, 31
	s_lshl_b64 s[12:13], s[12:13], 9
	v_lshl_add_u64 v[16:17], v[4:5], 0, s[12:13]
	v_lshl_add_u64 v[18:19], v[6:7], 0, s[12:13]
	v_readlane_b32 s12, v92, 5
	s_ashr_i32 s13, s12, 31
	s_lshl_b64 s[12:13], s[12:13], 9
	v_lshl_add_u64 v[20:21], v[6:7], 0, s[12:13]
	global_load_dwordx2 v[14:15], v[14:15], off
	s_nop 0
	global_load_dwordx2 v[16:17], v[16:17], off
	s_nop 0
	global_load_dwordx2 v[74:75], v[18:19], off
	global_load_dwordx2 v[70:71], v[20:21], off
	v_lshl_add_u64 v[18:19], v[4:5], 0, s[12:13]
	v_readlane_b32 s12, v92, 6
	s_ashr_i32 s13, s12, 31
	s_lshl_b64 s[12:13], s[12:13], 9
	v_lshl_add_u64 v[20:21], v[4:5], 0, s[12:13]
	v_lshl_add_u64 v[22:23], v[6:7], 0, s[12:13]
	v_readlane_b32 s12, v92, 7
	s_ashr_i32 s13, s12, 31
	s_lshl_b64 s[12:13], s[12:13], 9
	v_lshl_add_u64 v[24:25], v[6:7], 0, s[12:13]
	global_load_dwordx2 v[18:19], v[18:19], off
	s_nop 0
	global_load_dwordx2 v[20:21], v[20:21], off
	s_nop 0
	global_load_dwordx2 v[68:69], v[22:23], off
	global_load_dwordx2 v[64:65], v[24:25], off
	v_lshl_add_u64 v[22:23], v[4:5], 0, s[12:13]
	v_readlane_b32 s12, v92, 8
	s_ashr_i32 s13, s12, 31
	s_lshl_b64 s[12:13], s[12:13], 9
	v_lshl_add_u64 v[24:25], v[4:5], 0, s[12:13]
	v_lshl_add_u64 v[26:27], v[6:7], 0, s[12:13]
	v_readlane_b32 s12, v92, 9
	s_ashr_i32 s13, s12, 31
	s_lshl_b64 s[12:13], s[12:13], 9
	global_load_dwordx2 v[22:23], v[22:23], off
	s_nop 0
	global_load_dwordx2 v[24:25], v[24:25], off
	s_nop 0
	global_load_dwordx2 v[62:63], v[26:27], off
	v_lshl_add_u64 v[26:27], v[4:5], 0, s[12:13]
	global_load_dwordx2 v[38:39], v[26:27], off
	v_lshl_add_u64 v[26:27], v[6:7], 0, s[12:13]
	v_readlane_b32 s12, v92, 10
	s_ashr_i32 s13, s12, 31
	s_lshl_b64 s[12:13], s[12:13], 9
	global_load_dwordx2 v[66:67], v[26:27], off
	v_lshl_add_u64 v[26:27], v[4:5], 0, s[12:13]
	global_load_dwordx2 v[50:51], v[26:27], off
	v_lshl_add_u64 v[26:27], v[6:7], 0, s[12:13]
	v_readlane_b32 s12, v92, 11
	s_ashr_i32 s13, s12, 31
	s_lshl_b64 s[12:13], s[12:13], 9
	global_load_dwordx2 v[60:61], v[26:27], off
	v_lshl_add_u64 v[26:27], v[4:5], 0, s[12:13]
	global_load_dwordx2 v[48:49], v[26:27], off
	v_lshl_add_u64 v[26:27], v[6:7], 0, s[12:13]
	v_readlane_b32 s12, v92, 12
	s_ashr_i32 s13, s12, 31
	s_lshl_b64 s[12:13], s[12:13], 9
	global_load_dwordx2 v[58:59], v[26:27], off
	v_lshl_add_u64 v[26:27], v[4:5], 0, s[12:13]
	global_load_dwordx2 v[46:47], v[26:27], off
	v_lshl_add_u64 v[26:27], v[6:7], 0, s[12:13]
	v_readlane_b32 s12, v92, 13
	s_ashr_i32 s13, s12, 31
	s_lshl_b64 s[12:13], s[12:13], 9
	global_load_dwordx2 v[56:57], v[26:27], off
	v_lshl_add_u64 v[26:27], v[4:5], 0, s[12:13]
	global_load_dwordx2 v[44:45], v[26:27], off
	v_lshl_add_u64 v[26:27], v[6:7], 0, s[12:13]
	v_readlane_b32 s12, v92, 14
	s_ashr_i32 s13, s12, 31
	s_lshl_b64 s[12:13], s[12:13], 9
	global_load_dwordx2 v[54:55], v[26:27], off
	v_lshl_add_u64 v[26:27], v[4:5], 0, s[12:13]
	global_load_dwordx2 v[42:43], v[26:27], off
	v_lshl_add_u64 v[26:27], v[6:7], 0, s[12:13]
	v_readlane_b32 s12, v92, 15
	s_ashr_i32 s13, s12, 31
	s_lshl_b64 s[12:13], s[12:13], 9
	global_load_dwordx2 v[52:53], v[26:27], off
	v_lshl_add_u64 v[26:27], v[4:5], 0, s[12:13]
	global_load_dwordx2 v[40:41], v[26:27], off
	v_lshl_add_u64 v[26:27], v[6:7], 0, s[12:13]
	global_load_dwordx2 v[36:37], v[26:27], off
	v_readlane_b32 s12, v253, 15
	v_readlane_b32 s13, v253, 16
	s_nop 1
	v_lshl_add_u64 v[26:27], s[12:13], 0, v[144:145]
	v_readlane_b32 s12, v253, 13
	v_lshlrev_b32_e32 v144, 6, v28
	v_readlane_b32 s13, v253, 14
	s_waitcnt lgkmcnt(0)
	v_lshl_add_u64 v[30:31], s[10:11], 0, v[144:145]
	v_readlane_b32 s10, v253, 23
	v_lshl_add_u64 v[28:29], s[12:13], 0, v[144:145]
	v_readlane_b32 s12, v253, 2
	v_readlane_b32 s13, v253, 3
	v_readlane_b32 s11, v253, 24
	v_readlane_b32 s14, v253, 4
	v_lshl_add_u64 v[32:33], s[12:13], 0, v[144:145]
	v_lshl_add_u64 v[34:35], s[10:11], 0, v[34:35]
	s_mov_b64 s[10:11], 0
	v_lshlrev_b32_e32 v144, 2, v2
	v_readlane_b32 s15, v253, 5
	global_load_dwordx4 v[124:127], v[30:31], off
	global_load_dwordx4 v[128:131], v[30:31], off offset:16
	global_load_dwordx4 v[132:135], v[30:31], off offset:32
	global_load_dwordx4 v[136:139], v[30:31], off offset:48
.LBB0_762:
	v_ashrrev_i32_e32 v1, 31, v0
	v_lshlrev_b64 v[2:3], 6, v[0:1]
	v_lshl_add_u64 v[2:3], s[96:97], 0, v[2:3]
	global_load_dwordx4 v[84:87], v[2:3], off
	global_load_dwordx4 v[88:91], v[2:3], off offset:16
	v_lshlrev_b64 v[72:73], 11, v[0:1]
	global_load_dwordx4 v[94:97], v[2:3], off offset:32
	v_lshl_add_u64 v[72:73], v[26:27], 0, v[72:73]
	global_load_dwordx4 v[98:101], v[72:73], off
	global_load_dwordx4 v[102:105], v[72:73], off offset:16
	global_load_dwordx4 v[106:109], v[2:3], off offset:48
	s_mov_b32 s14, 0x42ee0000
	s_mov_b32 s58, 16
	s_waitcnt vmcnt(5)
	v_mov_b32_e32 v2, v85
	v_mov_b32_e32 v3, v86
	s_waitcnt vmcnt(4)
	v_mov_b32_e32 v72, v89
	v_mov_b32_e32 v73, v90
	v_mov_b32_e32 v85, v87
	v_mov_b32_e32 v89, v91
	s_waitcnt vmcnt(3)
	v_mov_b32_e32 v86, v95
	v_mov_b32_e32 v90, v97
	s_waitcnt vmcnt(2)
	v_lshlrev_b32_e32 v91, 16, v98
	v_pk_add_f32 v[2:3], v[2:3], v[84:85]
	v_pk_add_f32 v[72:73], v[72:73], v[88:89]
	v_pk_add_f32 v[84:85], v[94:95], v[86:87]
	v_pk_add_f32 v[86:87], v[96:97], v[90:91]
	v_pk_add_f32 v[2:3], v[2:3], v[2:3] op_sel:[0,1] op_sel_hi:[1,0]
	v_pk_add_f32 v[72:73], v[72:73], v[72:73] op_sel:[0,1] op_sel_hi:[1,0]
	s_waitcnt vmcnt(0)
	v_mov_b32_e32 v85, v108
	v_mov_b32_e32 v87, v109
	v_mov_b32_e32 v3, v106
	v_mov_b32_e32 v73, v107
	v_pk_add_f32 v[84:85], v[84:85], v[86:87]
	v_pk_add_f32 v[2:3], v[2:3], v[72:73]
	v_and_b32_e32 v98, 0xffff0000, v98
	v_pk_add_f32 v[2:3], v[2:3], v[84:85]
	v_lshlrev_b32_e32 v110, 16, v99
	v_add_f32_e32 v2, v2, v3
	v_fmamk_f32 v2, v2, 0x3a800000, v191
	v_mul_f32_e32 v3, 0x4b800000, v2
	v_cmp_gt_f32_e32 vcc, s18, v2
	v_and_b32_e32 v99, 0xffff0000, v99
	v_lshlrev_b32_e32 v111, 16, v100
	v_cndmask_b32_e32 v2, v2, v3, vcc
	v_rsq_f32_e32 v2, v2
	v_and_b32_e32 v100, 0xffff0000, v100
	v_lshlrev_b32_e32 v112, 16, v101
	v_and_b32_e32 v101, 0xffff0000, v101
	v_mul_f32_e32 v84, 0x45800000, v2
	v_cndmask_b32_e32 v2, v2, v84, vcc
	v_lshlrev_b32_e32 v113, 16, v102
	v_and_b32_e32 v102, 0xffff0000, v102
	v_lshlrev_b32_e32 v114, 16, v103
	v_and_b32_e32 v103, 0xffff0000, v103
	v_lshlrev_b32_e32 v115, 16, v104
	v_and_b32_e32 v3, 0xffff0000, v104
	v_lshlrev_b32_e32 v72, 16, v105
	v_and_b32_e32 v73, 0xffff0000, v105
	v_mul_f32_e32 v84, v2, v91
	v_mul_f32_e32 v85, v2, v98
	v_mul_f32_e32 v86, v2, v110
	v_mul_f32_e32 v87, v2, v99
	v_mul_f32_e32 v88, v2, v111
	v_mul_f32_e32 v89, v2, v100
	v_mul_f32_e32 v90, v2, v112
	v_mul_f32_e32 v91, v2, v101
	v_mul_f32_e32 v95, v2, v113
	v_mul_f32_e32 v96, v2, v102
	v_mul_f32_e32 v97, v2, v114
	v_mul_f32_e32 v98, v2, v103
	v_mul_f32_e32 v99, v2, v115
	v_mul_f32_e32 v100, v2, v3
	v_mul_f32_e32 v72, v2, v72
	v_mul_f32_e32 v73, v2, v73
	v_max_f32_e64 v2, |v84|, |v85|
	v_max_f32_e64 v3, |v86|, |v87|
	v_max_f32_e64 v94, |v88|, |v89|
	v_max_f32_e64 v101, |v90|, |v91|
	v_max3_f32 v2, v2, 0, v3
	v_max_f32_e64 v102, |v95|, |v96|
	v_max_f32_e64 v103, |v97|, |v98|
	v_max3_f32 v2, v2, v94, v101
	v_max_f32_e64 v104, |v99|, |v100|
	v_max_f32_e64 v105, |v72|, |v73|
	v_max3_f32 v2, v2, v102, v103
	v_max3_f32 v2, v2, v104, v105
	ds_bpermute_b32 v3, v184, v2
	v_add_u32_e32 v94, s86, v0
	v_cmp_gt_i32_e64 s[48:49], s87, v94
	s_waitcnt lgkmcnt(0)
	v_max_f32_e32 v3, v3, v3
	v_max_f32_e32 v2, v2, v3
	ds_bpermute_b32 v3, v185, v2
	s_waitcnt lgkmcnt(0)
	v_max_f32_e32 v3, v3, v3
	v_max_f32_e32 v2, v2, v3
	ds_bpermute_b32 v3, v186, v2
	s_waitcnt lgkmcnt(0)
	v_max_f32_e32 v3, v3, v3
	v_max_f32_e32 v2, v2, v3
	ds_bpermute_b32 v3, v187, v2
	s_waitcnt lgkmcnt(0)
	v_max_f32_e32 v3, v3, v3
	v_max_f32_e32 v2, v2, v3
	ds_bpermute_b32 v3, v188, v2
	s_waitcnt lgkmcnt(0)
	v_max_f32_e32 v3, v3, v3
	v_max_f32_e32 v101, v2, v3
	ds_bpermute_b32 v102, v189, v101
	v_lshlrev_b64 v[2:3], 10, v[0:1]
	v_lshlrev_b64 v[206:207], 2, v[2:3]
	v_lshl_add_u64 v[206:207], v[28:29], 0, v[206:207]
	global_load_dwordx4 v[208:211], v[206:207], off offset:48
	global_load_dwordx4 v[212:215], v[206:207], off offset:32
	global_load_dwordx4 v[216:219], v[206:207], off offset:16
	global_load_dwordx4 v[220:223], v[206:207], off
	s_waitcnt lgkmcnt(0)
	v_max_f32_e32 v1, v102, v102
	v_max_f32_e32 v101, v101, v1
	v_div_scale_f32 v1, s[12:13], v101, v101, s14
	v_rcp_f32_e32 v102, v1
	v_div_scale_f32 v103, vcc, s14, v101, s14
	s_movk_i32 s12, 0x3fff
	v_fma_f32 v104, -v1, v102, 1.0
	v_fmac_f32_e32 v102, v104, v102
	v_mul_f32_e32 v104, v103, v102
	v_fma_f32 v105, -v1, v104, v103
	v_fmac_f32_e32 v104, v105, v102
	v_fma_f32 v1, -v1, v104, v103
	v_div_fmas_f32 v1, v1, v102, v104
	v_div_fixup_f32 v1, v1, v101, s14
	v_cmp_lt_f32_e32 vcc, 0, v101
	v_cmp_lt_i32_e64 s[50:51], s12, v94
	s_or_b64 s[10:11], s[50:51], s[10:11]
	v_cndmask_b32_e32 v102, 0, v1, vcc
	v_mul_f32_e32 v1, v84, v102
	v_mul_f32_e32 v84, v85, v102
	v_mul_f32_e32 v85, v86, v102
	v_mul_f32_e32 v86, v87, v102
	v_rndne_f32_e32 v1, v1
	v_rndne_f32_e32 v84, v84
	v_mul_f32_e32 v87, v88, v102
	v_mul_f32_e32 v88, v89, v102
	v_rndne_f32_e32 v85, v85
	v_rndne_f32_e32 v86, v86
	v_cvt_i32_f32_e32 v1, v1
	v_cvt_i32_f32_e32 v84, v84
	v_rndne_f32_e32 v87, v87
	v_rndne_f32_e32 v88, v88
	v_cvt_i32_f32_e32 v85, v85
	v_cvt_i32_f32_e32 v86, v86
	v_cvt_i32_f32_e32 v87, v87
	v_cvt_i32_f32_e32 v88, v88
	v_mul_f32_e32 v89, v90, v102
	v_add_u32_e32 v90, 8, v1
	v_add_u32_e32 v104, 8, v84
	v_and_b32_e32 v103, 15, v1
	v_lshlrev_b32_e32 v105, 4, v84
	v_add_u32_e32 v1, v1, v84
	v_lshl_add_u32 v84, v85, 4, v196
	v_lshl_add_u32 v107, v86, 8, v200
	v_lshrrev_b32_e32 v90, 4, v90
	v_and_b32_e32 v104, 0xf0, v104
	v_lshl_add_u32 v109, v87, 12, v201
	v_lshl_add_u32 v111, v88, 16, v202
	v_and_b32_e32 v84, 0xf00, v84
	v_and_b32_e32 v107, 0xf000, v107
	v_and_or_b32 v90, v90, 15, v104
	v_lshlrev_b32_e32 v106, 8, v85
	v_add3_u32 v1, v1, v85, v86
	v_and_b32_e32 v85, 0xf0000, v109
	v_and_b32_e32 v109, 0xf00000, v111
	v_or3_b32 v84, v90, v84, v107
	v_lshlrev_b32_e32 v110, 16, v87
	v_or3_b32 v84, v84, v85, v109
	v_add3_u32 v85, v1, v87, v88
	v_mul_f32_e32 v87, v91, v102
	v_rndne_f32_e32 v89, v89
	v_rndne_f32_e32 v87, v87
	v_cvt_i32_f32_e32 v89, v89
	v_cvt_i32_f32_e32 v87, v87
	v_lshlrev_b32_e32 v108, 12, v86
	v_and_b32_e32 v105, 0xf0, v105
	v_lshl_add_u32 v1, v89, 20, v203
	v_lshl_add_u32 v90, v87, 24, v204
	v_and_b32_e32 v1, 0xf000000, v1
	v_and_b32_e32 v90, 0xf0000000, v90
	v_and_b32_e32 v106, 0xf00, v106
	v_or3_b32 v1, v84, v1, v90
	v_lshl_or_b32 v84, v87, 28, v103
	v_lshlrev_b32_e32 v112, 20, v88
	v_and_b32_e32 v108, 0xf000, v108
	v_and_b32_e32 v86, 0xf0000, v110
	v_lshlrev_b32_e32 v88, 24, v89
	v_or3_b32 v84, v84, v105, v106
	v_and_b32_e32 v110, 0xf00000, v112
	v_and_b32_e32 v88, 0xf000000, v88
	v_or3_b32 v84, v84, v108, v86
	v_or3_b32 v88, v84, v110, v88
	v_add3_u32 v84, v85, v89, v87
	v_mul_f32_e32 v85, v95, v102
	v_mul_f32_e32 v86, v96, v102
	v_rndne_f32_e32 v85, v85
	v_rndne_f32_e32 v86, v86
	v_cvt_i32_f32_e32 v85, v85
	v_cvt_i32_f32_e32 v86, v86
	v_mul_f32_e32 v95, v99, v102
	v_mul_f32_e32 v96, v100, v102
	v_add_u32_e32 v87, 8, v85
	v_add_u32_e32 v89, 8, v86
	v_lshrrev_b32_e32 v87, 4, v87
	v_and_b32_e32 v89, 0xf0, v89
	v_and_or_b32 v87, v87, 15, v89
	v_mul_f32_e32 v89, v97, v102
	v_lshlrev_b32_e32 v91, 4, v86
	v_add3_u32 v84, v84, v85, v86
	v_mul_f32_e32 v86, v98, v102
	v_rndne_f32_e32 v89, v89
	v_rndne_f32_e32 v86, v86
	v_cvt_i32_f32_e32 v89, v89
	v_cvt_i32_f32_e32 v86, v86
	v_rndne_f32_e32 v95, v95
	v_rndne_f32_e32 v96, v96
	v_mul_f32_e32 v72, v72, v102
	v_mul_f32_e32 v73, v73, v102
	v_cvt_i32_f32_e32 v95, v95
	v_cvt_i32_f32_e32 v96, v96
	v_rndne_f32_e32 v72, v72
	v_rndne_f32_e32 v73, v73
	v_cvt_i32_f32_e32 v72, v72
	v_cvt_i32_f32_e32 v73, v73
	v_add3_u32 v84, v84, v89, v86
	v_add3_u32 v84, v84, v95, v96
	v_and_b32_e32 v90, 15, v85
	v_add3_u32 v84, v84, v72, v73
	v_cvt_f32_i32_e32 v84, v84
	v_lshl_add_u32 v85, v89, 4, v196
	v_lshlrev_b32_e32 v89, 8, v89
	v_and_b32_e32 v97, 0xf00, v89
	ds_bpermute_b32 v98, v184, v84
	v_lshl_add_u32 v89, v86, 8, v200
	v_and_b32_e32 v85, 0xf00, v85
	v_and_b32_e32 v89, 0xf000, v89
	v_or3_b32 v85, v87, v85, v89
	s_waitcnt lgkmcnt(0)
	v_add_f32_e32 v84, v98, v84
	ds_bpermute_b32 v87, v185, v84
	v_lshl_add_u32 v89, v95, 12, v201
	v_lshl_add_u32 v98, v96, 16, v202
	v_and_b32_e32 v89, 0xf0000, v89
	v_and_b32_e32 v98, 0xf00000, v98
	s_waitcnt lgkmcnt(0)
	v_add_f32_e32 v84, v84, v87
	ds_bpermute_b32 v87, v186, v84
	v_or3_b32 v85, v85, v89, v98
	v_lshlrev_b32_e32 v89, 20, v96
	v_and_b32_e32 v96, 0xf00000, v89
	v_lshl_add_u32 v89, v72, 20, v203
	s_waitcnt lgkmcnt(0)
	v_add_f32_e32 v84, v84, v87
	ds_bpermute_b32 v87, v187, v84
	v_lshl_add_u32 v98, v73, 24, v204
	v_and_b32_e32 v89, 0xf000000, v89
	v_and_b32_e32 v98, 0xf0000000, v98
	v_or3_b32 v89, v85, v89, v98
	s_waitcnt lgkmcnt(0)
	v_add_f32_e32 v84, v84, v87
	ds_bpermute_b32 v87, v188, v84
	v_and_b32_e32 v91, 0xf0, v91
	v_lshlrev_b32_e32 v86, 12, v86
	v_lshlrev_b32_e32 v95, 16, v95
	v_lshl_or_b32 v73, v73, 28, v90
	s_waitcnt lgkmcnt(0)
	v_add_f32_e32 v84, v84, v87
	ds_bpermute_b32 v85, v189, v84
	v_and_b32_e32 v86, 0xf000, v86
	v_and_b32_e32 v95, 0xf0000, v95
	v_lshlrev_b32_e32 v72, 24, v72
	v_or3_b32 v73, v73, v91, v97
	v_and_b32_e32 v72, 0xf000000, v72
	v_or3_b32 v73, v73, v86, v95
	v_or3_b32 v90, v73, v96, v72
	s_waitcnt lgkmcnt(0)
	v_add_f32_e32 v72, v84, v85
	v_mul_f32_e32 v91, 0x3c09ae41, v101
	v_mul_f32_e32 v95, 0.5, v72
	v_mov_b32_e32 v103, 0
	v_mov_b64_e32 v[72:73], v[34:35]
	v_mov_b32_e32 v102, 0
	v_mov_b32_e32 v101, 0
	v_mov_b32_e32 v100, 0
	v_mov_b32_e32 v99, 0
	v_mov_b32_e32 v98, 0
	v_mov_b32_e32 v97, 0
	v_mov_b32_e32 v96, 0
.LBB0_763:
	s_cmpk_eq_i32 s58, 0x80
	s_cselect_b64 s[12:13], -1, 0
	ds_bpermute_b32 v84, v93, v92
	s_and_b64 vcc, s[12:13], s[48:49]
	v_cndmask_b32_e32 v104, v0, v94, vcc
	v_ashrrev_i32_e32 v105, 31, v104
	s_and_b32 s12, s58, 0x70
	v_lshlrev_b64 v[104:105], 9, v[104:105]
	v_lshl_add_u64 v[104:105], s[94:95], 0, v[104:105]
	s_lshl_b32 s36, s12, 2
	s_waitcnt lgkmcnt(0)
	v_ashrrev_i32_e32 v85, 31, v84
	v_lshl_add_u64 v[104:105], v[104:105], 0, s[36:37]
	v_lshl_add_u64 v[84:85], v[84:85], 3, s[8:9]
	v_lshl_add_u64 v[104:105], v[104:105], 0, v[144:145]
	global_load_dwordx2 v[84:85], v[84:85], off
	s_nop 0
	global_load_dword v86, v[72:73], off
	global_load_dword v92, v[104:105], off
	s_waitcnt vmcnt(11)
	v_dot8_i32_i4 v87, v8, v1, 0
	v_dot8_i32_i4 v104, v8, v88, 0
	v_dot8_i32_i4 v87, v9, v89, v87
	v_dot8_i32_i4 v104, v9, v90, v104
	s_waitcnt vmcnt(10)
	v_dot8_i32_i4 v9, v10, v88, 0
	v_dot8_i32_i4 v9, v11, v90, v9
	v_lshl_add_u32 v8, v87, 4, v104
	v_cvt_f32_i32_e32 v87, v8
	v_dot8_i32_i4 v8, v10, v1, 0
	v_dot8_i32_i4 v8, v11, v89, v8
	s_add_i32 s58, s58, 16
	v_lshl_add_u64 v[72:73], v[72:73], 0, 64
	s_waitcnt vmcnt(2)
	v_mul_f32_e32 v85, v91, v85
	v_lshl_add_u32 v8, v8, 4, v9
	v_cvt_f32_i32_e32 v104, v8
	v_dot8_i32_i4 v8, v12, v1, 0
	v_dot8_i32_i4 v9, v12, v88, 0
	v_dot8_i32_i4 v8, v13, v89, v8
	v_dot8_i32_i4 v9, v13, v90, v9
	s_waitcnt vmcnt(0)
	v_readlane_b32 s12, v92, 0
	v_readlane_b32 s28, v92, 8
	v_readlane_b32 s30, v92, 9
	v_lshl_add_u32 v8, v8, 4, v9
	v_cvt_f32_i32_e32 v105, v8
	v_dot8_i32_i4 v8, v14, v1, 0
	v_dot8_i32_i4 v9, v14, v88, 0
	v_dot8_i32_i4 v8, v15, v89, v8
	v_dot8_i32_i4 v9, v15, v90, v9
	s_ashr_i32 s13, s12, 31
	v_readlane_b32 s14, v92, 1
	s_ashr_i32 s29, s28, 31
	v_lshl_add_u32 v8, v8, 4, v9
	v_cvt_f32_i32_e32 v106, v8
	v_dot8_i32_i4 v8, v16, v1, 0
	v_dot8_i32_i4 v9, v16, v88, 0
	v_dot8_i32_i4 v8, v17, v89, v8
	v_dot8_i32_i4 v9, v17, v90, v9
	s_ashr_i32 s31, s30, 31
	v_readlane_b32 s34, v92, 10
	s_lshl_b64 s[12:13], s[12:13], 9
	v_lshl_add_u32 v8, v8, 4, v9
	v_cvt_f32_i32_e32 v107, v8
	v_dot8_i32_i4 v8, v18, v1, 0
	v_dot8_i32_i4 v9, v18, v88, 0
	v_dot8_i32_i4 v8, v19, v89, v8
	v_dot8_i32_i4 v9, v19, v90, v9
	s_ashr_i32 s15, s14, 31
	v_readlane_b32 s16, v92, 2
	s_lshl_b64 s[28:29], s[28:29], 9
	v_lshl_add_u32 v8, v8, 4, v9
	v_cvt_f32_i32_e32 v108, v8
	v_dot8_i32_i4 v8, v20, v1, 0
	v_dot8_i32_i4 v9, v20, v88, 0
	v_dot8_i32_i4 v8, v21, v89, v8
	v_dot8_i32_i4 v9, v21, v90, v9
	s_lshl_b64 s[30:31], s[30:31], 9
	s_ashr_i32 s35, s34, 31
	v_readlane_b32 s38, v92, 11
	v_lshl_add_u32 v8, v8, 4, v9
	v_cvt_f32_i32_e32 v109, v8
	v_dot8_i32_i4 v8, v22, v1, 0
	v_dot8_i32_i4 v9, v22, v88, 0
	v_dot8_i32_i4 v8, v23, v89, v8
	v_dot8_i32_i4 v9, v23, v90, v9
	s_lshl_b64 s[14:15], s[14:15], 9
	s_ashr_i32 s17, s16, 31
	v_readlane_b32 s18, v92, 3
	v_lshl_add_u32 v8, v8, 4, v9
	v_cvt_f32_i32_e32 v110, v8
	v_dot8_i32_i4 v8, v24, v1, 0
	v_dot8_i32_i4 v9, v24, v88, 0
	v_dot8_i32_i4 v8, v25, v89, v8
	v_dot8_i32_i4 v9, v25, v90, v9
	v_lshl_add_u64 v[24:25], v[4:5], 0, s[28:29]
	s_lshl_b64 s[34:35], s[34:35], 9
	s_ashr_i32 s39, s38, 31
	v_lshl_add_u32 v8, v8, 4, v9
	v_cvt_f32_i32_e32 v111, v8
	v_dot8_i32_i4 v8, v38, v1, 0
	v_dot8_i32_i4 v9, v38, v88, 0
	v_dot8_i32_i4 v8, v39, v89, v8
	v_dot8_i32_i4 v9, v39, v90, v9
	v_cndmask_b32_e64 v119, v87, v111, s[40:41]
	v_cndmask_b32_e64 v87, v111, v87, s[40:41]
	ds_bpermute_b32 v111, v184, v119
	v_lshl_add_u32 v8, v8, 4, v9
	v_cvt_f32_i32_e32 v112, v8
	v_dot8_i32_i4 v8, v50, v1, 0
	v_dot8_i32_i4 v9, v50, v88, 0
	v_dot8_i32_i4 v8, v51, v89, v8
	v_dot8_i32_i4 v9, v51, v90, v9
	s_waitcnt lgkmcnt(0)
	v_add_f32_e32 v87, v87, v111
	v_cndmask_b32_e64 v111, v104, v112, s[40:41]
	ds_bpermute_b32 v111, v184, v111
	v_lshl_add_u32 v8, v8, 4, v9
	v_cvt_f32_i32_e32 v113, v8
	v_dot8_i32_i4 v8, v48, v1, 0
	v_dot8_i32_i4 v9, v48, v88, 0
	v_cndmask_b32_e64 v104, v112, v104, s[40:41]
	v_dot8_i32_i4 v8, v49, v89, v8
	v_dot8_i32_i4 v9, v49, v90, v9
	s_waitcnt lgkmcnt(0)
	v_add_f32_e32 v104, v104, v111
	v_cndmask_b32_e64 v111, v105, v113, s[40:41]
	ds_bpermute_b32 v111, v184, v111
	v_lshl_add_u32 v8, v8, 4, v9
	v_cvt_f32_i32_e32 v114, v8
	v_dot8_i32_i4 v8, v46, v1, 0
	v_dot8_i32_i4 v9, v46, v88, 0
	v_cndmask_b32_e64 v105, v113, v105, s[40:41]
	v_dot8_i32_i4 v8, v47, v89, v8
	v_dot8_i32_i4 v9, v47, v90, v9
	s_waitcnt lgkmcnt(0)
	v_add_f32_e32 v105, v105, v111
	v_cndmask_b32_e64 v111, v106, v114, s[40:41]
	ds_bpermute_b32 v111, v184, v111
	v_lshl_add_u32 v8, v8, 4, v9
	v_cvt_f32_i32_e32 v115, v8
	v_dot8_i32_i4 v8, v44, v1, 0
	v_dot8_i32_i4 v9, v44, v88, 0
	v_cndmask_b32_e64 v106, v114, v106, s[40:41]
	v_dot8_i32_i4 v8, v45, v89, v8
	v_dot8_i32_i4 v9, v45, v90, v9
	s_waitcnt lgkmcnt(0)
	v_add_f32_e32 v106, v106, v111
	v_cndmask_b32_e64 v111, v107, v115, s[40:41]
	ds_bpermute_b32 v111, v184, v111
	v_lshl_add_u32 v8, v8, 4, v9
	v_cvt_f32_i32_e32 v116, v8
	v_dot8_i32_i4 v8, v42, v1, 0
	v_dot8_i32_i4 v9, v42, v88, 0
	v_cndmask_b32_e64 v107, v115, v107, s[40:41]
	v_dot8_i32_i4 v8, v43, v89, v8
	v_dot8_i32_i4 v9, v43, v90, v9
	s_waitcnt lgkmcnt(0)
	v_add_f32_e32 v107, v107, v111
	v_cndmask_b32_e64 v111, v108, v116, s[40:41]
	ds_bpermute_b32 v111, v184, v111
	v_lshl_add_u32 v8, v8, 4, v9
	v_cvt_f32_i32_e32 v117, v8
	v_dot8_i32_i4 v8, v40, v1, 0
	v_dot8_i32_i4 v9, v40, v88, 0
	v_cndmask_b32_e64 v108, v116, v108, s[40:41]
	v_dot8_i32_i4 v8, v41, v89, v8
	v_dot8_i32_i4 v9, v41, v90, v9
	s_waitcnt lgkmcnt(0)
	v_add_f32_e32 v108, v108, v111
	v_cndmask_b32_e64 v111, v109, v117, s[40:41]
	ds_bpermute_b32 v111, v184, v111
	v_lshl_add_u32 v8, v8, 4, v9
	v_cvt_f32_i32_e32 v118, v8
	v_cndmask_b32_e64 v109, v117, v109, s[40:41]
	v_lshl_add_u64 v[38:39], v[4:5], 0, s[30:31]
	s_waitcnt lgkmcnt(0)
	v_add_f32_e32 v109, v109, v111
	v_cndmask_b32_e64 v111, v110, v118, s[40:41]
	ds_bpermute_b32 v111, v184, v111
	v_cndmask_b32_e64 v110, v118, v110, s[40:41]
	v_readlane_b32 s50, v92, 12
	s_lshl_b64 s[16:17], s[16:17], 9
	s_ashr_i32 s19, s18, 31
	s_waitcnt lgkmcnt(0)
	v_add_f32_e32 v110, v110, v111
	v_cndmask_b32_e64 v111, v87, v107, s[42:43]
	v_cndmask_b32_e64 v87, v107, v87, s[42:43]
	ds_bpermute_b32 v107, v185, v111
	v_readlane_b32 s20, v92, 4
	global_load_dwordx2 v[24:25], v[24:25], off
	v_lshl_add_u64 v[40:41], v[4:5], 0, s[34:35]
	global_load_dwordx2 v[38:39], v[38:39], off
	s_waitcnt lgkmcnt(0)
	v_add_f32_e32 v87, v87, v107
	v_cndmask_b32_e64 v107, v104, v108, s[42:43]
	ds_bpermute_b32 v107, v185, v107
	v_cndmask_b32_e64 v104, v108, v104, s[42:43]
	s_lshl_b64 s[38:39], s[38:39], 9
	s_ashr_i32 s51, s50, 31
	v_readlane_b32 s52, v92, 13
	s_waitcnt lgkmcnt(0)
	v_add_f32_e32 v104, v104, v107
	v_cndmask_b32_e64 v107, v105, v109, s[42:43]
	ds_bpermute_b32 v107, v185, v107
	v_cndmask_b32_e64 v105, v109, v105, s[42:43]
	s_lshl_b64 s[18:19], s[18:19], 9
	s_ashr_i32 s21, s20, 31
	v_readlane_b32 s22, v92, 5
	s_waitcnt lgkmcnt(0)
	v_add_f32_e32 v105, v105, v107
	v_cndmask_b32_e64 v107, v106, v110, s[42:43]
	ds_bpermute_b32 v107, v185, v107
	v_cndmask_b32_e64 v106, v110, v106, s[42:43]
	global_load_dwordx2 v[50:51], v[40:41], off
	s_lshl_b64 s[50:51], s[50:51], 9
	s_ashr_i32 s53, s52, 31
	s_waitcnt lgkmcnt(0)
	v_add_f32_e32 v106, v106, v107
	v_cndmask_b32_e64 v107, v87, v105, s[44:45]
	v_cndmask_b32_e64 v87, v105, v87, s[44:45]
	ds_bpermute_b32 v105, v186, v107
	v_readlane_b32 s54, v92, 14
	s_lshl_b64 s[20:21], s[20:21], 9
	s_ashr_i32 s23, s22, 31
	v_readlane_b32 s24, v92, 6
	s_waitcnt lgkmcnt(0)
	v_add_f32_e32 v87, v87, v105
	v_cndmask_b32_e64 v105, v104, v106, s[44:45]
	ds_bpermute_b32 v105, v186, v105
	v_cndmask_b32_e64 v104, v106, v104, s[44:45]
	s_lshl_b64 s[52:53], s[52:53], 9
	s_ashr_i32 s55, s54, 31
	v_readlane_b32 s56, v92, 15
	s_waitcnt lgkmcnt(0)
	v_add_f32_e32 v104, v104, v105
	v_cndmask_b32_e64 v105, v87, v104, s[46:47]
	v_cndmask_b32_e64 v87, v104, v87, s[46:47]
	ds_bpermute_b32 v104, v187, v105
	s_lshl_b64 s[22:23], s[22:23], 9
	s_ashr_i32 s25, s24, 31
	v_readlane_b32 s26, v92, 7
	s_lshl_b64 s[54:55], s[54:55], 9
	s_waitcnt lgkmcnt(0)
	v_add_f32_e32 v87, v87, v104
	ds_bpermute_b32 v104, v188, v87
	s_ashr_i32 s57, s56, 31
	s_lshl_b64 s[24:25], s[24:25], 9
	s_ashr_i32 s27, s26, 31
	s_lshl_b64 s[56:57], s[56:57], 9
	s_waitcnt lgkmcnt(0)
	v_add_f32_e32 v87, v87, v104
	ds_bpermute_b32 v104, v189, v87
	s_lshl_b64 s[26:27], s[26:27], 9
	v_lshl_add_u64 v[8:9], v[4:5], 0, s[12:13]
	v_lshl_add_u64 v[10:11], v[4:5], 0, s[14:15]
	v_lshl_add_u64 v[12:13], v[4:5], 0, s[16:17]
	s_waitcnt lgkmcnt(0)
	v_add_f32_e32 v87, v87, v104
	v_add_f32_e32 v87, v95, v87
	v_mul_f32_e32 v85, v85, v87
	v_mul_f32_e32 v87, 0x3d372713, v85
	v_mul_f32_e32 v87, v85, v87
	v_fma_f32 v87, v85, v87, v85
	v_mul_f32_e32 v87, 0x3fcc422a, v87
	v_mul_f32_e32 v87, 0xbfb8aa3b, v87
	v_exp_f32_e32 v87, v87
	v_lshlrev_b32_e32 v104, 4, v82
	v_lshl_add_u64 v[14:15], v[4:5], 0, s[18:19]
	v_lshl_add_u64 v[16:17], v[4:5], 0, s[20:21]
	v_add_f32_e32 v87, 1.0, v87
	v_rcp_f32_e32 v87, v87
	v_lshl_add_u64 v[18:19], v[4:5], 0, s[22:23]
	v_lshl_add_u64 v[20:21], v[4:5], 0, s[24:25]
	v_lshl_add_u64 v[22:23], v[4:5], 0, s[26:27]
	v_pk_mul_f32 v[84:85], v[84:85], v[86:87]
	v_lshrrev_b32_e32 v87, 4, v82
	v_pk_mul_f32 v[84:85], v[84:85], v[84:85] op_sel:[0,1] op_sel_hi:[1,0]
	v_cvt_f16_f32_e32 v120, v84
	v_and_b32_e32 v86, 0x7070707, v82
	v_readlane_b32 s36, v120, 0
	v_and_b32_e32 v87, 0x7070707, v87
	v_perm_b32 v86, s2, v205, v86
	v_perm_b32 v87, s2, v205, v87
	v_and_or_b32 v86, v104, s4, v86
	v_and_or_b32 v82, v82, s4, v87
	v_perm_b32 v87, v82, v86, s5
	v_perm_b32 v104, v82, v86, s33
	v_perm_b32 v105, v82, v86, s0
	v_perm_b32 v82, v82, v86, s1
	v_pk_fma_f16 v86, v87, s36, v103 op_sel_hi:[1,0,1]
	v_pk_fma_f16 v87, v104, s36, v102 op_sel_hi:[1,0,1]
	v_lshrrev_b32_e32 v102, 4, v83
	v_pk_fma_f16 v82, v82, s36, v100 op_sel_hi:[1,0,1]
	v_and_b32_e32 v100, 0x7070707, v83
	v_and_b32_e32 v102, 0x7070707, v102
	v_perm_b32 v100, s2, v205, v100
	v_perm_b32 v102, s2, v205, v102
	v_lshlrev_b32_e32 v103, 4, v83
	v_and_or_b32 v100, v103, s4, v100
	v_and_or_b32 v83, v83, s4, v102
	v_perm_b32 v102, v83, v100, s5
	v_perm_b32 v103, v83, v100, s33
	v_perm_b32 v104, v83, v100, s0
	v_perm_b32 v83, v83, v100, s1
	v_readlane_b32 s59, v120, 4
	v_lshrrev_b32_e32 v100, 4, v80
	v_pk_fma_f16 v101, v105, s36, v101 op_sel_hi:[1,0,1]
	v_pk_fma_f16 v99, v102, s36, v99 op_sel_hi:[1,0,1]
	v_pk_fma_f16 v98, v103, s36, v98 op_sel_hi:[1,0,1]
	v_pk_fma_f16 v97, v104, s36, v97 op_sel_hi:[1,0,1]
	v_pk_fma_f16 v83, v83, s36, v96 op_sel_hi:[1,0,1]
	v_and_b32_e32 v96, 0x7070707, v80
	v_and_b32_e32 v100, 0x7070707, v100
	v_perm_b32 v96, s2, v205, v96
	v_perm_b32 v100, s2, v205, v100
	v_lshlrev_b32_e32 v102, 4, v80
	v_and_or_b32 v96, v102, s4, v96
	v_and_or_b32 v80, v80, s4, v100
	v_perm_b32 v100, v80, v96, s5
	v_perm_b32 v102, v80, v96, s33
	v_perm_b32 v103, v80, v96, s0
	v_perm_b32 v80, v80, v96, s1
	v_pk_fma_f16 v86, v100, s59, v86 op_sel_hi:[1,0,1]
	v_lshrrev_b32_e32 v100, 4, v81
	v_pk_fma_f16 v80, v80, s59, v82 op_sel_hi:[1,0,1]
	v_and_b32_e32 v82, 0x7070707, v81
	v_and_b32_e32 v100, 0x7070707, v100
	v_pk_fma_f16 v96, v103, s59, v101 op_sel_hi:[1,0,1]
	v_perm_b32 v82, s2, v205, v82
	v_perm_b32 v100, s2, v205, v100
	v_lshlrev_b32_e32 v101, 4, v81
	v_and_or_b32 v82, v101, s4, v82
	v_and_or_b32 v81, v81, s4, v100
	v_perm_b32 v100, v81, v82, s5
	v_pk_fma_f16 v87, v102, s59, v87 op_sel_hi:[1,0,1]
	v_perm_b32 v101, v81, v82, s33
	v_perm_b32 v102, v81, v82, s0
	v_perm_b32 v81, v81, v82, s1
	v_pk_fma_f16 v82, v100, s59, v99 op_sel_hi:[1,0,1]
	v_readlane_b32 s60, v120, 8
	v_lshrrev_b32_e32 v99, 4, v78
	v_pk_fma_f16 v98, v101, s59, v98 op_sel_hi:[1,0,1]
	v_pk_fma_f16 v97, v102, s59, v97 op_sel_hi:[1,0,1]
	v_pk_fma_f16 v81, v81, s59, v83 op_sel_hi:[1,0,1]
	v_and_b32_e32 v85, 0x7070707, v78
	v_and_b32_e32 v99, 0x7070707, v99
	v_perm_b32 v85, s2, v205, v85
	v_perm_b32 v99, s2, v205, v99
	v_lshlrev_b32_e32 v100, 4, v78
	v_and_or_b32 v85, v100, s4, v85
	v_and_or_b32 v78, v78, s4, v99
	v_perm_b32 v99, v78, v85, s5
	v_perm_b32 v100, v78, v85, s33
	v_perm_b32 v101, v78, v85, s0
	v_perm_b32 v78, v78, v85, s1
	v_pk_fma_f16 v85, v99, s60, v86 op_sel_hi:[1,0,1]
	v_pk_fma_f16 v86, v100, s60, v87 op_sel_hi:[1,0,1]
	v_pk_fma_f16 v87, v101, s60, v96 op_sel_hi:[1,0,1]
	v_lshrrev_b32_e32 v96, 4, v79
	v_pk_fma_f16 v78, v78, s60, v80 op_sel_hi:[1,0,1]
	v_and_b32_e32 v80, 0x7070707, v79
	v_and_b32_e32 v96, 0x7070707, v96
	v_perm_b32 v80, s2, v205, v80
	v_perm_b32 v96, s2, v205, v96
	v_lshlrev_b32_e32 v99, 4, v79
	v_and_or_b32 v80, v99, s4, v80
	v_and_or_b32 v79, v79, s4, v96
	v_perm_b32 v96, v79, v80, s5
	v_perm_b32 v100, v79, v80, s0
	v_perm_b32 v99, v79, v80, s33
	v_perm_b32 v79, v79, v80, s1
	v_pk_fma_f16 v80, v96, s60, v82 op_sel_hi:[1,0,1]
	v_pk_fma_f16 v96, v100, s60, v97 op_sel_hi:[1,0,1]
	v_readlane_b32 s36, v120, 12
	v_lshrrev_b32_e32 v97, 4, v76
	v_pk_fma_f16 v82, v99, s60, v98 op_sel_hi:[1,0,1]
	v_pk_fma_f16 v79, v79, s60, v81 op_sel_hi:[1,0,1]
	v_and_b32_e32 v83, 0x7070707, v76
	v_and_b32_e32 v97, 0x7070707, v97
	v_perm_b32 v83, s2, v205, v83
	v_perm_b32 v97, s2, v205, v97
	v_lshlrev_b32_e32 v98, 4, v76
	v_and_or_b32 v83, v98, s4, v83
	v_and_or_b32 v76, v76, s4, v97
	v_perm_b32 v97, v76, v83, s5
	v_perm_b32 v98, v76, v83, s33
	v_perm_b32 v99, v76, v83, s0
	v_perm_b32 v76, v76, v83, s1
	v_pk_fma_f16 v83, v97, s36, v85 op_sel_hi:[1,0,1]
	v_pk_fma_f16 v85, v98, s36, v86 op_sel_hi:[1,0,1]
	v_pk_fma_f16 v86, v99, s36, v87 op_sel_hi:[1,0,1]
	v_lshrrev_b32_e32 v87, 4, v77
	v_pk_fma_f16 v76, v76, s36, v78 op_sel_hi:[1,0,1]
	v_and_b32_e32 v78, 0x7070707, v77
	v_and_b32_e32 v87, 0x7070707, v87
	v_perm_b32 v78, s2, v205, v78
	v_perm_b32 v87, s2, v205, v87
	v_lshlrev_b32_e32 v97, 4, v77
	v_and_or_b32 v78, v97, s4, v78
	v_and_or_b32 v77, v77, s4, v87
	v_perm_b32 v87, v77, v78, s5
	v_perm_b32 v97, v77, v78, s33
	v_perm_b32 v98, v77, v78, s0
	v_perm_b32 v77, v77, v78, s1
	v_pk_fma_f16 v78, v87, s36, v80 op_sel_hi:[1,0,1]
	v_readlane_b32 s59, v120, 16
	v_lshrrev_b32_e32 v87, 4, v74
	v_pk_fma_f16 v80, v97, s36, v82 op_sel_hi:[1,0,1]
	v_pk_fma_f16 v82, v98, s36, v96 op_sel_hi:[1,0,1]
	v_pk_fma_f16 v77, v77, s36, v79 op_sel_hi:[1,0,1]
	v_and_b32_e32 v81, 0x7070707, v74
	v_and_b32_e32 v87, 0x7070707, v87
	v_perm_b32 v81, s2, v205, v81
	v_perm_b32 v87, s2, v205, v87
	v_lshlrev_b32_e32 v96, 4, v74
	v_and_or_b32 v81, v96, s4, v81
	v_and_or_b32 v74, v74, s4, v87
	v_perm_b32 v87, v74, v81, s5
	v_perm_b32 v96, v74, v81, s33
	v_perm_b32 v97, v74, v81, s0
	v_perm_b32 v74, v74, v81, s1
	v_pk_fma_f16 v81, v87, s59, v83 op_sel_hi:[1,0,1]
	v_pk_fma_f16 v83, v96, s59, v85 op_sel_hi:[1,0,1]
	v_pk_fma_f16 v85, v97, s59, v86 op_sel_hi:[1,0,1]
	v_lshrrev_b32_e32 v86, 4, v75
	v_pk_fma_f16 v74, v74, s59, v76 op_sel_hi:[1,0,1]
	v_and_b32_e32 v76, 0x7070707, v75
	v_and_b32_e32 v86, 0x7070707, v86
	v_perm_b32 v76, s2, v205, v76
	v_perm_b32 v86, s2, v205, v86
	v_lshlrev_b32_e32 v87, 4, v75
	v_and_or_b32 v76, v87, s4, v76
	v_and_or_b32 v75, v75, s4, v86
	v_perm_b32 v86, v75, v76, s5
	v_perm_b32 v87, v75, v76, s33
	v_perm_b32 v96, v75, v76, s0
	v_perm_b32 v75, v75, v76, s1
	v_pk_fma_f16 v76, v86, s59, v78 op_sel_hi:[1,0,1]
	v_pk_fma_f16 v78, v87, s59, v80 op_sel_hi:[1,0,1]
	v_pk_fma_f16 v80, v96, s59, v82 op_sel_hi:[1,0,1]
	v_readlane_b32 s60, v120, 20
	v_lshrrev_b32_e32 v82, 4, v70
	v_pk_fma_f16 v75, v75, s59, v77 op_sel_hi:[1,0,1]
	v_and_b32_e32 v79, 0x7070707, v70
	v_and_b32_e32 v82, 0x7070707, v82
	v_perm_b32 v79, s2, v205, v79
	v_perm_b32 v82, s2, v205, v82
	v_lshlrev_b32_e32 v86, 4, v70
	v_and_or_b32 v79, v86, s4, v79
	v_and_or_b32 v70, v70, s4, v82
	v_perm_b32 v82, v70, v79, s5
	v_perm_b32 v86, v70, v79, s33
	v_perm_b32 v87, v70, v79, s0
	v_perm_b32 v70, v70, v79, s1
	v_pk_fma_f16 v79, v82, s60, v81 op_sel_hi:[1,0,1]
	v_pk_fma_f16 v81, v86, s60, v83 op_sel_hi:[1,0,1]
	v_lshrrev_b32_e32 v83, 4, v71
	v_pk_fma_f16 v70, v70, s60, v74 op_sel_hi:[1,0,1]
	v_and_b32_e32 v74, 0x7070707, v71
	v_and_b32_e32 v83, 0x7070707, v83
	v_pk_fma_f16 v82, v87, s60, v85 op_sel_hi:[1,0,1]
	v_perm_b32 v74, s2, v205, v74
	v_perm_b32 v83, s2, v205, v83
	v_lshlrev_b32_e32 v85, 4, v71
	v_and_or_b32 v74, v85, s4, v74
	v_and_or_b32 v71, v71, s4, v83
	v_perm_b32 v83, v71, v74, s5
	v_perm_b32 v85, v71, v74, s33
	v_perm_b32 v86, v71, v74, s0
	v_perm_b32 v71, v71, v74, s1
	v_pk_fma_f16 v74, v83, s60, v76 op_sel_hi:[1,0,1]
	v_pk_fma_f16 v76, v85, s60, v78 op_sel_hi:[1,0,1]
	v_pk_fma_f16 v78, v86, s60, v80 op_sel_hi:[1,0,1]
	v_readlane_b32 s36, v120, 24
	v_lshrrev_b32_e32 v80, 4, v68
	v_pk_fma_f16 v71, v71, s60, v75 op_sel_hi:[1,0,1]
	v_and_b32_e32 v77, 0x7070707, v68
	v_and_b32_e32 v80, 0x7070707, v80
	v_perm_b32 v77, s2, v205, v77
	v_perm_b32 v80, s2, v205, v80
	v_lshlrev_b32_e32 v83, 4, v68
	v_and_or_b32 v77, v83, s4, v77
	v_and_or_b32 v68, v68, s4, v80
	v_perm_b32 v80, v68, v77, s5
	v_perm_b32 v83, v68, v77, s33
	v_perm_b32 v85, v68, v77, s0
	v_perm_b32 v68, v68, v77, s1
	v_pk_fma_f16 v77, v80, s36, v79 op_sel_hi:[1,0,1]
	v_pk_fma_f16 v79, v83, s36, v81 op_sel_hi:[1,0,1]
	v_lshrrev_b32_e32 v81, 4, v69
	v_pk_fma_f16 v68, v68, s36, v70 op_sel_hi:[1,0,1]
	v_and_b32_e32 v70, 0x7070707, v69
	v_and_b32_e32 v81, 0x7070707, v81
	v_pk_fma_f16 v80, v85, s36, v82 op_sel_hi:[1,0,1]
	v_perm_b32 v70, s2, v205, v70
	v_perm_b32 v81, s2, v205, v81
	v_lshlrev_b32_e32 v82, 4, v69
	v_and_or_b32 v70, v82, s4, v70
	v_and_or_b32 v69, v69, s4, v81
	v_perm_b32 v81, v69, v70, s5
	v_perm_b32 v82, v69, v70, s33
	v_perm_b32 v83, v69, v70, s0
	v_perm_b32 v69, v69, v70, s1
	v_pk_fma_f16 v70, v81, s36, v74 op_sel_hi:[1,0,1]
	v_pk_fma_f16 v74, v82, s36, v76 op_sel_hi:[1,0,1]
	v_pk_fma_f16 v76, v83, s36, v78 op_sel_hi:[1,0,1]
	v_readlane_b32 s59, v120, 28
	v_lshrrev_b32_e32 v78, 4, v64
	v_pk_fma_f16 v69, v69, s36, v71 op_sel_hi:[1,0,1]
	v_and_b32_e32 v75, 0x7070707, v64
	v_and_b32_e32 v78, 0x7070707, v78
	v_perm_b32 v75, s2, v205, v75
	v_perm_b32 v78, s2, v205, v78
	v_lshlrev_b32_e32 v81, 4, v64
	v_and_or_b32 v75, v81, s4, v75
	v_and_or_b32 v64, v64, s4, v78
	v_perm_b32 v78, v64, v75, s5
	v_perm_b32 v81, v64, v75, s33
	v_perm_b32 v82, v64, v75, s0
	v_perm_b32 v64, v64, v75, s1
	v_pk_fma_f16 v75, v78, s59, v77 op_sel_hi:[1,0,1]
	v_pk_fma_f16 v77, v81, s59, v79 op_sel_hi:[1,0,1]
	v_lshrrev_b32_e32 v79, 4, v65
	v_pk_fma_f16 v64, v64, s59, v68 op_sel_hi:[1,0,1]
	v_and_b32_e32 v68, 0x7070707, v65
	v_and_b32_e32 v79, 0x7070707, v79
	v_pk_fma_f16 v78, v82, s59, v80 op_sel_hi:[1,0,1]
	v_perm_b32 v68, s2, v205, v68
	v_perm_b32 v79, s2, v205, v79
	v_lshlrev_b32_e32 v80, 4, v65
	v_and_or_b32 v68, v80, s4, v68
	v_and_or_b32 v65, v65, s4, v79
	v_perm_b32 v79, v65, v68, s5
	v_perm_b32 v80, v65, v68, s33
	v_perm_b32 v81, v65, v68, s0
	v_perm_b32 v65, v65, v68, s1
	v_pk_fma_f16 v68, v79, s59, v70 op_sel_hi:[1,0,1]
	v_pk_fma_f16 v70, v80, s59, v74 op_sel_hi:[1,0,1]
	v_pk_fma_f16 v74, v81, s59, v76 op_sel_hi:[1,0,1]
	v_readlane_b32 s60, v120, 32
	v_lshrrev_b32_e32 v76, 4, v62
	v_pk_fma_f16 v65, v65, s59, v69 op_sel_hi:[1,0,1]
	v_and_b32_e32 v71, 0x7070707, v62
	v_and_b32_e32 v76, 0x7070707, v76
	v_perm_b32 v71, s2, v205, v71
	v_perm_b32 v76, s2, v205, v76
	v_lshlrev_b32_e32 v79, 4, v62
	v_and_or_b32 v71, v79, s4, v71
	v_and_or_b32 v62, v62, s4, v76
	v_perm_b32 v76, v62, v71, s5
	v_perm_b32 v79, v62, v71, s33
	v_perm_b32 v80, v62, v71, s0
	v_perm_b32 v62, v62, v71, s1
	v_pk_fma_f16 v71, v76, s60, v75 op_sel_hi:[1,0,1]
	v_pk_fma_f16 v75, v79, s60, v77 op_sel_hi:[1,0,1]
	v_lshrrev_b32_e32 v77, 4, v63
	v_pk_fma_f16 v62, v62, s60, v64 op_sel_hi:[1,0,1]
	v_and_b32_e32 v64, 0x7070707, v63
	v_and_b32_e32 v77, 0x7070707, v77
	v_pk_fma_f16 v76, v80, s60, v78 op_sel_hi:[1,0,1]
	v_perm_b32 v64, s2, v205, v64
	v_perm_b32 v77, s2, v205, v77
	v_lshlrev_b32_e32 v78, 4, v63
	v_and_or_b32 v64, v78, s4, v64
	v_and_or_b32 v63, v63, s4, v77
	v_perm_b32 v77, v63, v64, s5
	v_perm_b32 v78, v63, v64, s33
	v_perm_b32 v79, v63, v64, s0
	v_perm_b32 v63, v63, v64, s1
	v_pk_fma_f16 v64, v77, s60, v68 op_sel_hi:[1,0,1]
	v_pk_fma_f16 v68, v78, s60, v70 op_sel_hi:[1,0,1]
	v_pk_fma_f16 v70, v79, s60, v74 op_sel_hi:[1,0,1]
	v_readlane_b32 s36, v120, 36
	v_lshrrev_b32_e32 v74, 4, v66
	v_pk_fma_f16 v63, v63, s60, v65 op_sel_hi:[1,0,1]
	v_and_b32_e32 v69, 0x7070707, v66
	v_and_b32_e32 v74, 0x7070707, v74
	v_perm_b32 v69, s2, v205, v69
	v_perm_b32 v74, s2, v205, v74
	v_lshlrev_b32_e32 v77, 4, v66
	v_and_or_b32 v69, v77, s4, v69
	v_and_or_b32 v66, v66, s4, v74
	v_perm_b32 v74, v66, v69, s5
	v_perm_b32 v77, v66, v69, s33
	v_perm_b32 v78, v66, v69, s0
	v_perm_b32 v66, v66, v69, s1
	v_pk_fma_f16 v69, v74, s36, v71 op_sel_hi:[1,0,1]
	v_pk_fma_f16 v71, v77, s36, v75 op_sel_hi:[1,0,1]
	v_lshrrev_b32_e32 v75, 4, v67
	v_pk_fma_f16 v62, v66, s36, v62 op_sel_hi:[1,0,1]
	v_and_b32_e32 v66, 0x7070707, v67
	v_and_b32_e32 v75, 0x7070707, v75
	v_pk_fma_f16 v74, v78, s36, v76 op_sel_hi:[1,0,1]
	v_perm_b32 v66, s2, v205, v66
	v_perm_b32 v75, s2, v205, v75
	v_lshlrev_b32_e32 v76, 4, v67
	v_and_or_b32 v66, v76, s4, v66
	v_and_or_b32 v67, v67, s4, v75
	v_perm_b32 v76, v67, v66, s33
	v_perm_b32 v77, v67, v66, s0
	v_perm_b32 v75, v67, v66, s5
	v_perm_b32 v66, v67, v66, s1
	v_pk_fma_f16 v67, v76, s36, v68 op_sel_hi:[1,0,1]
	v_pk_fma_f16 v68, v77, s36, v70 op_sel_hi:[1,0,1]
	v_readlane_b32 s59, v120, 40
	v_lshrrev_b32_e32 v70, 4, v60
	v_pk_fma_f16 v64, v75, s36, v64 op_sel_hi:[1,0,1]
	v_pk_fma_f16 v63, v66, s36, v63 op_sel_hi:[1,0,1]
	v_and_b32_e32 v66, 0x7070707, v60
	v_and_b32_e32 v70, 0x7070707, v70
	v_perm_b32 v66, s2, v205, v66
	v_perm_b32 v70, s2, v205, v70
	v_lshlrev_b32_e32 v75, 4, v60
	v_and_or_b32 v66, v75, s4, v66
	v_and_or_b32 v60, v60, s4, v70
	v_perm_b32 v70, v60, v66, s5
	v_perm_b32 v75, v60, v66, s33
	v_perm_b32 v76, v60, v66, s0
	v_perm_b32 v60, v60, v66, s1
	v_pk_fma_f16 v66, v70, s59, v69 op_sel_hi:[1,0,1]
	v_pk_fma_f16 v69, v75, s59, v71 op_sel_hi:[1,0,1]
	v_lshrrev_b32_e32 v71, 4, v61
	v_pk_fma_f16 v60, v60, s59, v62 op_sel_hi:[1,0,1]
	v_and_b32_e32 v62, 0x7070707, v61
	v_and_b32_e32 v71, 0x7070707, v71
	v_pk_fma_f16 v70, v76, s59, v74 op_sel_hi:[1,0,1]
	v_perm_b32 v62, s2, v205, v62
	v_perm_b32 v71, s2, v205, v71
	v_lshlrev_b32_e32 v74, 4, v61
	v_and_or_b32 v62, v74, s4, v62
	v_and_or_b32 v61, v61, s4, v71
	v_perm_b32 v71, v61, v62, s5
	v_perm_b32 v74, v61, v62, s33
	v_perm_b32 v75, v61, v62, s0
	v_perm_b32 v61, v61, v62, s1
	v_pk_fma_f16 v62, v71, s59, v64 op_sel_hi:[1,0,1]
	v_pk_fma_f16 v64, v74, s59, v67 op_sel_hi:[1,0,1]
	v_pk_fma_f16 v67, v75, s59, v68 op_sel_hi:[1,0,1]
	v_readlane_b32 s60, v120, 44
	v_lshrrev_b32_e32 v68, 4, v58
	v_pk_fma_f16 v61, v61, s59, v63 op_sel_hi:[1,0,1]
	v_and_b32_e32 v65, 0x7070707, v58
	v_and_b32_e32 v68, 0x7070707, v68
	v_perm_b32 v65, s2, v205, v65
	v_perm_b32 v68, s2, v205, v68
	v_lshlrev_b32_e32 v71, 4, v58
	v_and_or_b32 v65, v71, s4, v65
	v_and_or_b32 v58, v58, s4, v68
	v_perm_b32 v68, v58, v65, s5
	v_perm_b32 v71, v58, v65, s33
	v_perm_b32 v74, v58, v65, s0
	v_perm_b32 v58, v58, v65, s1
	v_pk_fma_f16 v65, v68, s60, v66 op_sel_hi:[1,0,1]
	v_pk_fma_f16 v66, v71, s60, v69 op_sel_hi:[1,0,1]
	v_lshrrev_b32_e32 v69, 4, v59
	v_pk_fma_f16 v58, v58, s60, v60 op_sel_hi:[1,0,1]
	v_and_b32_e32 v60, 0x7070707, v59
	v_and_b32_e32 v69, 0x7070707, v69
	v_pk_fma_f16 v68, v74, s60, v70 op_sel_hi:[1,0,1]
	v_perm_b32 v60, s2, v205, v60
	v_perm_b32 v69, s2, v205, v69
	v_lshlrev_b32_e32 v70, 4, v59
	v_and_or_b32 v60, v70, s4, v60
	v_and_or_b32 v59, v59, s4, v69
	v_perm_b32 v69, v59, v60, s5
	v_perm_b32 v70, v59, v60, s33
	v_perm_b32 v71, v59, v60, s0
	v_perm_b32 v59, v59, v60, s1
	v_pk_fma_f16 v60, v69, s60, v62 op_sel_hi:[1,0,1]
	v_pk_fma_f16 v62, v70, s60, v64 op_sel_hi:[1,0,1]
	v_pk_fma_f16 v64, v71, s60, v67 op_sel_hi:[1,0,1]
	v_readlane_b32 s36, v120, 48
	v_lshrrev_b32_e32 v67, 4, v56
	v_pk_fma_f16 v59, v59, s60, v61 op_sel_hi:[1,0,1]
	v_and_b32_e32 v63, 0x7070707, v56
	v_and_b32_e32 v67, 0x7070707, v67
	v_perm_b32 v63, s2, v205, v63
	v_perm_b32 v67, s2, v205, v67
	v_lshlrev_b32_e32 v69, 4, v56
	v_and_or_b32 v63, v69, s4, v63
	v_and_or_b32 v56, v56, s4, v67
	v_perm_b32 v67, v56, v63, s5
	v_perm_b32 v69, v56, v63, s33
	v_perm_b32 v70, v56, v63, s0
	v_perm_b32 v56, v56, v63, s1
	v_pk_fma_f16 v63, v67, s36, v65 op_sel_hi:[1,0,1]
	v_lshrrev_b32_e32 v67, 4, v57
	v_pk_fma_f16 v56, v56, s36, v58 op_sel_hi:[1,0,1]
	v_and_b32_e32 v58, 0x7070707, v57
	v_and_b32_e32 v67, 0x7070707, v67
	v_pk_fma_f16 v65, v69, s36, v66 op_sel_hi:[1,0,1]
	v_pk_fma_f16 v66, v70, s36, v68 op_sel_hi:[1,0,1]
	v_perm_b32 v58, s2, v205, v58
	v_perm_b32 v67, s2, v205, v67
	v_lshlrev_b32_e32 v68, 4, v57
	v_and_or_b32 v58, v68, s4, v58
	v_and_or_b32 v57, v57, s4, v67
	v_perm_b32 v67, v57, v58, s5
	v_perm_b32 v68, v57, v58, s33
	v_perm_b32 v69, v57, v58, s0
	v_perm_b32 v57, v57, v58, s1
	v_pk_fma_f16 v58, v67, s36, v60 op_sel_hi:[1,0,1]
	v_pk_fma_f16 v60, v68, s36, v62 op_sel_hi:[1,0,1]
	v_pk_fma_f16 v62, v69, s36, v64 op_sel_hi:[1,0,1]
	v_readlane_b32 s59, v120, 52
	v_lshrrev_b32_e32 v64, 4, v54
	v_pk_fma_f16 v57, v57, s36, v59 op_sel_hi:[1,0,1]
	v_and_b32_e32 v61, 0x7070707, v54
	v_and_b32_e32 v64, 0x7070707, v64
	v_perm_b32 v61, s2, v205, v61
	v_perm_b32 v64, s2, v205, v64
	v_lshlrev_b32_e32 v67, 4, v54
	v_and_or_b32 v61, v67, s4, v61
	v_and_or_b32 v54, v54, s4, v64
	v_perm_b32 v64, v54, v61, s5
	v_perm_b32 v67, v54, v61, s33
	v_perm_b32 v68, v54, v61, s0
	v_perm_b32 v54, v54, v61, s1
	v_pk_fma_f16 v61, v64, s59, v63 op_sel_hi:[1,0,1]
	v_pk_fma_f16 v63, v67, s59, v65 op_sel_hi:[1,0,1]
	v_lshrrev_b32_e32 v65, 4, v55
	v_pk_fma_f16 v54, v54, s59, v56 op_sel_hi:[1,0,1]
	v_and_b32_e32 v56, 0x7070707, v55
	v_and_b32_e32 v65, 0x7070707, v65
	v_pk_fma_f16 v64, v68, s59, v66 op_sel_hi:[1,0,1]
	v_perm_b32 v56, s2, v205, v56
	v_perm_b32 v65, s2, v205, v65
	v_lshlrev_b32_e32 v66, 4, v55
	v_and_or_b32 v56, v66, s4, v56
	v_and_or_b32 v55, v55, s4, v65
	v_perm_b32 v65, v55, v56, s5
	v_perm_b32 v66, v55, v56, s33
	v_perm_b32 v67, v55, v56, s0
	v_perm_b32 v55, v55, v56, s1
	v_pk_fma_f16 v56, v65, s59, v58 op_sel_hi:[1,0,1]
	v_pk_fma_f16 v58, v66, s59, v60 op_sel_hi:[1,0,1]
	v_pk_fma_f16 v60, v67, s59, v62 op_sel_hi:[1,0,1]
	v_readlane_b32 s60, v120, 56
	v_lshrrev_b32_e32 v62, 4, v52
	v_pk_fma_f16 v55, v55, s59, v57 op_sel_hi:[1,0,1]
	v_and_b32_e32 v59, 0x7070707, v52
	v_and_b32_e32 v62, 0x7070707, v62
	v_perm_b32 v59, s2, v205, v59
	v_perm_b32 v62, s2, v205, v62
	v_lshlrev_b32_e32 v65, 4, v52
	v_and_or_b32 v59, v65, s4, v59
	v_and_or_b32 v52, v52, s4, v62
	v_perm_b32 v62, v52, v59, s5
	v_perm_b32 v65, v52, v59, s33
	v_perm_b32 v66, v52, v59, s0
	v_perm_b32 v52, v52, v59, s1
	v_pk_fma_f16 v59, v62, s60, v61 op_sel_hi:[1,0,1]
	v_pk_fma_f16 v61, v65, s60, v63 op_sel_hi:[1,0,1]
	v_lshrrev_b32_e32 v63, 4, v53
	v_pk_fma_f16 v52, v52, s60, v54 op_sel_hi:[1,0,1]
	v_and_b32_e32 v54, 0x7070707, v53
	v_and_b32_e32 v63, 0x7070707, v63
	v_pk_fma_f16 v62, v66, s60, v64 op_sel_hi:[1,0,1]
	v_perm_b32 v54, s2, v205, v54
	v_perm_b32 v63, s2, v205, v63
	v_lshlrev_b32_e32 v64, 4, v53
	v_and_or_b32 v54, v64, s4, v54
	v_and_or_b32 v53, v53, s4, v63
	v_perm_b32 v63, v53, v54, s5
	v_perm_b32 v64, v53, v54, s33
	v_perm_b32 v65, v53, v54, s0
	v_perm_b32 v53, v53, v54, s1
	v_pk_fma_f16 v54, v63, s60, v56 op_sel_hi:[1,0,1]
	v_pk_fma_f16 v56, v64, s60, v58 op_sel_hi:[1,0,1]
	v_pk_fma_f16 v58, v65, s60, v60 op_sel_hi:[1,0,1]
	v_readlane_b32 s36, v120, 60
	v_lshrrev_b32_e32 v60, 4, v36
	v_pk_fma_f16 v53, v53, s60, v55 op_sel_hi:[1,0,1]
	v_and_b32_e32 v57, 0x7070707, v36
	v_and_b32_e32 v60, 0x7070707, v60
	v_perm_b32 v57, s2, v205, v57
	v_perm_b32 v60, s2, v205, v60
	v_lshlrev_b32_e32 v63, 4, v36
	v_and_or_b32 v57, v63, s4, v57
	v_and_or_b32 v36, v36, s4, v60
	v_perm_b32 v60, v36, v57, s5
	v_perm_b32 v63, v36, v57, s33
	v_perm_b32 v64, v36, v57, s0
	v_perm_b32 v36, v36, v57, s1
	v_pk_fma_f16 v100, v36, s36, v52 op_sel_hi:[1,0,1]
	v_lshrrev_b32_e32 v52, 4, v37
	v_and_b32_e32 v36, 0x7070707, v37
	v_and_b32_e32 v52, 0x7070707, v52
	v_perm_b32 v36, s2, v205, v36
	v_perm_b32 v52, s2, v205, v52
	v_lshlrev_b32_e32 v57, 4, v37
	v_and_or_b32 v36, v57, s4, v36
	v_and_or_b32 v37, v37, s4, v52
	v_pk_fma_f16 v103, v60, s36, v59 op_sel_hi:[1,0,1]
	v_perm_b32 v52, v37, v36, s5
	v_perm_b32 v57, v37, v36, s33
	v_perm_b32 v59, v37, v36, s0
	v_perm_b32 v36, v37, v36, s1
	v_pk_fma_f16 v96, v36, s36, v53 op_sel_hi:[1,0,1]
	v_lshl_add_u64 v[36:37], v[6:7], 0, s[12:13]
	global_load_dwordx2 v[82:83], v[36:37], off
	v_lshl_add_u64 v[36:37], v[6:7], 0, s[14:15]
	global_load_dwordx2 v[80:81], v[36:37], off
	v_lshl_add_u64 v[40:41], v[4:5], 0, s[38:39]
	v_lshl_add_u64 v[36:37], v[6:7], 0, s[16:17]
	global_load_dwordx2 v[48:49], v[40:41], off
	global_load_dwordx2 v[78:79], v[36:37], off
	v_lshl_add_u64 v[40:41], v[4:5], 0, s[50:51]
	v_lshl_add_u64 v[36:37], v[6:7], 0, s[18:19]
	global_load_dwordx2 v[46:47], v[40:41], off
	global_load_dwordx2 v[76:77], v[36:37], off
	v_lshl_add_u64 v[40:41], v[4:5], 0, s[52:53]
	v_lshl_add_u64 v[36:37], v[6:7], 0, s[20:21]
	global_load_dwordx2 v[44:45], v[40:41], off
	global_load_dwordx2 v[74:75], v[36:37], off
	v_lshl_add_u64 v[40:41], v[4:5], 0, s[54:55]
	v_lshl_add_u64 v[36:37], v[6:7], 0, s[22:23]
	global_load_dwordx2 v[42:43], v[40:41], off
	global_load_dwordx2 v[70:71], v[36:37], off
	v_lshl_add_u64 v[40:41], v[4:5], 0, s[56:57]
	v_lshl_add_u64 v[36:37], v[6:7], 0, s[24:25]
	global_load_dwordx2 v[40:41], v[40:41], off
	v_pk_fma_f16 v101, v64, s36, v62 op_sel_hi:[1,0,1]
	global_load_dwordx2 v[68:69], v[36:37], off
	v_lshl_add_u64 v[36:37], v[6:7], 0, s[26:27]
	global_load_dwordx2 v[64:65], v[36:37], off
	v_lshl_add_u64 v[36:37], v[6:7], 0, s[28:29]
	v_pk_fma_f16 v102, v63, s36, v61 op_sel_hi:[1,0,1]
	global_load_dwordx2 v[62:63], v[36:37], off
	v_lshl_add_u64 v[36:37], v[6:7], 0, s[30:31]
	global_load_dwordx2 v[66:67], v[36:37], off
	v_lshl_add_u64 v[36:37], v[6:7], 0, s[34:35]
	global_load_dwordx2 v[60:61], v[36:37], off
	v_lshl_add_u64 v[36:37], v[6:7], 0, s[38:39]
	v_pk_fma_f16 v97, v59, s36, v58 op_sel_hi:[1,0,1]
	global_load_dwordx2 v[58:59], v[36:37], off
	v_lshl_add_u64 v[36:37], v[6:7], 0, s[50:51]
	v_pk_fma_f16 v98, v57, s36, v56 op_sel_hi:[1,0,1]
	global_load_dwordx2 v[56:57], v[36:37], off
	v_lshl_add_u64 v[36:37], v[6:7], 0, s[52:53]
	v_pk_fma_f16 v99, v52, s36, v54 op_sel_hi:[1,0,1]
	global_load_dwordx2 v[54:55], v[36:37], off
	v_lshl_add_u64 v[36:37], v[6:7], 0, s[54:55]
	global_load_dwordx2 v[52:53], v[36:37], off
	v_lshl_add_u64 v[36:37], v[6:7], 0, s[56:57]
	global_load_dwordx2 v[8:9], v[8:9], off
	s_cmpk_eq_i32 s58, 0x90
	global_load_dwordx2 v[10:11], v[10:11], off
	s_nop 0
	global_load_dwordx2 v[12:13], v[12:13], off
	s_nop 0
	global_load_dwordx2 v[14:15], v[14:15], off
	s_nop 0
	global_load_dwordx2 v[16:17], v[16:17], off
	s_nop 0
	global_load_dwordx2 v[18:19], v[18:19], off
	s_nop 0
	global_load_dwordx2 v[20:21], v[20:21], off
	s_nop 0
	global_load_dwordx2 v[22:23], v[22:23], off
	s_nop 0
	global_load_dwordx2 v[36:37], v[36:37], off
	s_cbranch_scc0 .LBB0_763
	v_lshlrev_b64 v[0:1], 2, v[2:3]
	v_lshl_add_u64 v[2:3], v[28:29], 0, v[0:1]
	v_mov_b32_e32 v104, v208
	v_mov_b32_e32 v105, v209
	v_mov_b32_e32 v106, v210
	v_mov_b32_e32 v107, v211
	v_mov_b32_e32 v108, v212
	v_mov_b32_e32 v109, v213
	v_mov_b32_e32 v110, v214
	v_mov_b32_e32 v111, v215
	v_mov_b32_e32 v86, v216
	v_mov_b32_e32 v87, v217
	v_mov_b32_e32 v88, v218
	v_mov_b32_e32 v89, v219
	v_mov_b32_e32 v112, v220
	v_mov_b32_e32 v113, v221
	v_mov_b32_e32 v114, v222
	v_mov_b32_e32 v115, v223
	v_lshl_add_u64 v[72:73], v[32:33], 0, v[0:1]
	v_cvt_f32_f16_sdwa v1, v103 dst_sel:DWORD dst_unused:UNUSED_PAD src0_sel:WORD_1
	v_cvt_f32_f16_e32 v0, v103
	v_cvt_f32_f16_sdwa v91, v102 dst_sel:DWORD dst_unused:UNUSED_PAD src0_sel:WORD_1
	v_cvt_f32_f16_e32 v90, v102
	v_cvt_f32_f16_sdwa v103, v101 dst_sel:DWORD dst_unused:UNUSED_PAD src0_sel:WORD_1
	v_cvt_f32_f16_e32 v102, v101
	v_cvt_f32_f16_sdwa v101, v100 dst_sel:DWORD dst_unused:UNUSED_PAD src0_sel:WORD_1
	v_cvt_f32_f16_e32 v100, v100
	s_mov_b32 s18, 0x800000
	v_readlane_b32 s12, v255, 5
	v_readlane_b32 s13, v255, 6
	v_pk_add_f32 v[86:87], v[86:87], v[102:103]
	v_pk_add_f32 v[84:85], v[112:113], v[0:1]
	v_mov_b32_e32 v102, v85
	v_mov_b32_e32 v103, v87
	v_pk_add_f32 v[90:91], v[114:115], v[90:91]
	v_pk_add_f32 v[88:89], v[88:89], v[100:101]
	v_mov_b32_e32 v100, v84
	v_mov_b32_e32 v101, v86
	v_pk_mul_f32 v[102:103], v[102:103], v[102:103]
	v_mov_b32_e32 v112, v91
	v_pk_fma_f32 v[100:101], v[100:101], v[100:101], v[102:103]
	v_mov_b32_e32 v102, v90
	v_mov_b32_e32 v103, v88
	v_pk_fma_f32 v[100:101], v[102:103], v[102:103], v[100:101]
	v_cvt_f32_f16_sdwa v103, v99 dst_sel:DWORD dst_unused:UNUSED_PAD src0_sel:WORD_1
	v_cvt_f32_f16_e32 v102, v99
	v_cvt_f32_f16_sdwa v99, v98 dst_sel:DWORD dst_unused:UNUSED_PAD src0_sel:WORD_1
	v_cvt_f32_f16_e32 v98, v98
	v_mov_b32_e32 v113, v89
	v_pk_add_f32 v[102:103], v[108:109], v[102:103]
	v_cvt_f32_f16_sdwa v109, v97 dst_sel:DWORD dst_unused:UNUSED_PAD src0_sel:WORD_1
	v_cvt_f32_f16_e32 v108, v97
	v_cvt_f32_f16_sdwa v97, v96 dst_sel:DWORD dst_unused:UNUSED_PAD src0_sel:WORD_1
	v_cvt_f32_f16_e32 v96, v96
	v_pk_add_f32 v[98:99], v[110:111], v[98:99]
	v_pk_add_f32 v[104:105], v[104:105], v[108:109]
	v_mov_b32_e32 v108, v103
	v_mov_b32_e32 v109, v105
	v_pk_add_f32 v[96:97], v[106:107], v[96:97]
	v_mov_b32_e32 v106, v102
	v_mov_b32_e32 v107, v104
	v_pk_mul_f32 v[108:109], v[108:109], v[108:109]
	v_pk_fma_f32 v[100:101], v[112:113], v[112:113], v[100:101]
	v_pk_fma_f32 v[106:107], v[106:107], v[106:107], v[108:109]
	v_mov_b32_e32 v108, v98
	v_mov_b32_e32 v109, v96
	v_mov_b32_e32 v110, v99
	v_mov_b32_e32 v111, v97
	v_pk_fma_f32 v[106:107], v[108:109], v[108:109], v[106:107]
	v_add_f32_e32 v95, v100, v101
	v_pk_fma_f32 v[106:107], v[110:111], v[110:111], v[106:107]
	v_lshl_add_u64 v[34:35], v[34:35], 0, s[12:13]
	v_add_f32_e32 v95, v95, v106
	v_add_f32_e32 v95, v95, v107
	ds_bpermute_b32 v100, v184, v95
	s_waitcnt lgkmcnt(0)
	v_add_f32_e32 v95, v95, v100
	ds_bpermute_b32 v100, v185, v95
	s_waitcnt lgkmcnt(0)
	v_add_f32_e32 v95, v95, v100
	ds_bpermute_b32 v100, v186, v95
	s_waitcnt lgkmcnt(0)
	v_add_f32_e32 v95, v95, v100
	ds_bpermute_b32 v100, v187, v95
	s_waitcnt lgkmcnt(0)
	v_add_f32_e32 v95, v95, v100
	ds_bpermute_b32 v100, v188, v95
	s_waitcnt lgkmcnt(0)
	v_add_f32_e32 v95, v95, v100
	ds_bpermute_b32 v100, v189, v95
	s_waitcnt lgkmcnt(0)
	v_add_f32_e32 v95, v95, v100
	v_fmamk_f32 v95, v95, 0x3a800000, v191
	v_cmp_gt_f32_e32 vcc, s18, v95
	v_mul_f32_e32 v100, 0x4b800000, v95
	s_nop 0
	v_cndmask_b32_e32 v95, v95, v100, vcc
	v_rsq_f32_e32 v95, v95
	s_nop 0
	v_mul_f32_e32 v100, 0x45800000, v95
	v_cndmask_b32_e32 v100, v95, v100, vcc
	v_pk_mul_f32 v[84:85], v[84:85], v[100:101] op_sel_hi:[1,0]
	v_pk_mul_f32 v[0:1], v[124:125], v[84:85]
	v_pk_mul_f32 v[84:85], v[90:91], v[100:101] op_sel_hi:[1,0]
	s_nop 0
	v_pk_mul_f32 v[2:3], v[126:127], v[84:85]
	global_store_dwordx4 v[72:73], v[0:3], off
	s_nop 1
	v_pk_mul_f32 v[84:85], v[86:87], v[100:101] op_sel_hi:[1,0]
	v_pk_mul_f32 v[0:1], v[128:129], v[84:85]
	v_pk_mul_f32 v[84:85], v[88:89], v[100:101] op_sel_hi:[1,0]
	s_nop 0
	v_pk_mul_f32 v[2:3], v[130:131], v[84:85]
	global_store_dwordx4 v[72:73], v[0:3], off offset:16
	s_nop 1
	v_pk_mul_f32 v[84:85], v[102:103], v[100:101] op_sel_hi:[1,0]
	v_pk_mul_f32 v[0:1], v[84:85], v[132:133]
	v_pk_mul_f32 v[84:85], v[98:99], v[100:101] op_sel_hi:[1,0]
	s_nop 0
	v_pk_mul_f32 v[2:3], v[84:85], v[134:135]
	global_store_dwordx4 v[72:73], v[0:3], off offset:32
	s_nop 1
	v_pk_mul_f32 v[84:85], v[104:105], v[100:101] op_sel_hi:[1,0]
	v_pk_mul_f32 v[0:1], v[84:85], v[136:137]
	v_pk_mul_f32 v[84:85], v[96:97], v[100:101] op_sel_hi:[1,0]
	s_nop 0
	v_pk_mul_f32 v[2:3], v[84:85], v[138:139]
	global_store_dwordx4 v[72:73], v[0:3], off offset:48
	s_nop 1
	v_mov_b32_e32 v0, v94
	s_andn2_b64 exec, exec, s[10:11]
	s_cbranch_execnz .LBB0_762

.LBB0_769:
	v_ashrrev_i32_e32 v1, 31, v0
	v_lshlrev_b64 v[2:3], 6, v[0:1]
	v_lshl_add_u64 v[14:15], s[96:97], 0, v[2:3]
	global_load_dwordx4 v[2:5], v[14:15], off
	global_load_dwordx4 v[6:9], v[14:15], off offset:16
	v_lshlrev_b64 v[74:75], 11, v[0:1]
	global_load_dwordx4 v[10:13], v[14:15], off offset:32
	v_lshl_add_u64 v[74:75], v[42:43], 0, v[74:75]
	global_load_dwordx4 v[98:101], v[74:75], off
	global_load_dwordx4 v[102:105], v[74:75], off offset:16
	global_load_dwordx4 v[106:109], v[14:15], off offset:48
	s_mov_b32 s56, 16
	s_waitcnt vmcnt(5)
	v_mov_b32_e32 v14, v3
	v_mov_b32_e32 v15, v4
	s_waitcnt vmcnt(4)
	v_mov_b32_e32 v94, v7
	v_mov_b32_e32 v95, v8
	v_mov_b32_e32 v3, v5
	v_mov_b32_e32 v7, v9
	s_waitcnt vmcnt(3)
	v_mov_b32_e32 v4, v11
	v_mov_b32_e32 v8, v13
	v_pk_add_f32 v[2:3], v[14:15], v[2:3]
	v_pk_add_f32 v[6:7], v[94:95], v[6:7]
	v_pk_add_f32 v[4:5], v[10:11], v[4:5]
	v_pk_add_f32 v[8:9], v[12:13], v[8:9]
	v_pk_add_f32 v[2:3], v[2:3], v[2:3] op_sel:[0,1] op_sel_hi:[1,0]
	v_pk_add_f32 v[6:7], v[6:7], v[6:7] op_sel:[0,1] op_sel_hi:[1,0]
	s_waitcnt vmcnt(0)
	v_mov_b32_e32 v5, v108
	v_mov_b32_e32 v9, v109
	v_mov_b32_e32 v3, v106
	v_mov_b32_e32 v7, v107
	v_pk_add_f32 v[4:5], v[4:5], v[8:9]
	v_pk_add_f32 v[2:3], v[2:3], v[6:7]
	v_lshlrev_b32_e32 v110, 16, v98
	v_pk_add_f32 v[2:3], v[2:3], v[4:5]
	v_and_b32_e32 v98, 0xffff0000, v98
	v_add_f32_e32 v2, v2, v3
	v_fmamk_f32 v2, v2, 0x3a800000, v191
	v_mul_f32_e32 v3, 0x4b800000, v2
	v_cmp_gt_f32_e32 vcc, s12, v2
	v_lshlrev_b32_e32 v111, 16, v99
	v_and_b32_e32 v99, 0xffff0000, v99
	v_cndmask_b32_e32 v2, v2, v3, vcc
	v_rsq_f32_e32 v2, v2
	v_lshlrev_b32_e32 v112, 16, v100
	v_and_b32_e32 v100, 0xffff0000, v100
	v_lshlrev_b32_e32 v113, 16, v101
	v_mul_f32_e32 v6, 0x45800000, v2
	v_cndmask_b32_e32 v2, v2, v6, vcc
	v_and_b32_e32 v101, 0xffff0000, v101
	v_lshlrev_b32_e32 v114, 16, v102
	v_and_b32_e32 v102, 0xffff0000, v102
	v_lshlrev_b32_e32 v115, 16, v103
	v_and_b32_e32 v103, 0xffff0000, v103
	v_lshlrev_b32_e32 v116, 16, v104
	v_and_b32_e32 v3, 0xffff0000, v104
	v_lshlrev_b32_e32 v4, 16, v105
	v_and_b32_e32 v5, 0xffff0000, v105
	v_mul_f32_e32 v6, v2, v110
	v_mul_f32_e32 v7, v2, v98
	v_mul_f32_e32 v8, v2, v111
	v_mul_f32_e32 v9, v2, v99
	v_mul_f32_e32 v10, v2, v112
	v_mul_f32_e32 v11, v2, v100
	v_mul_f32_e32 v12, v2, v113
	v_mul_f32_e32 v13, v2, v101
	v_mul_f32_e32 v14, v2, v114
	v_mul_f32_e32 v15, v2, v102
	v_mul_f32_e32 v94, v2, v115
	v_mul_f32_e32 v95, v2, v103
	v_mul_f32_e32 v99, v2, v116
	v_mul_f32_e32 v100, v2, v3
	v_mul_f32_e32 v4, v2, v4
	v_mul_f32_e32 v5, v2, v5
	v_max_f32_e64 v2, |v6|, |v7|
	v_max_f32_e64 v3, |v8|, |v9|
	v_max_f32_e64 v98, |v10|, |v11|
	v_max_f32_e64 v101, |v12|, |v13|
	v_max3_f32 v2, v2, 0, v3
	v_max_f32_e64 v102, |v14|, |v15|
	v_max_f32_e64 v103, |v94|, |v95|
	v_max3_f32 v2, v2, v98, v101
	v_max_f32_e64 v104, |v99|, |v100|
	v_max_f32_e64 v105, |v4|, |v5|
	v_max3_f32 v2, v2, v102, v103
	v_max3_f32 v2, v2, v104, v105
	ds_bpermute_b32 v3, v184, v2
	s_mov_b32 s12, 0x42ee0000
	v_add_u32_e32 v98, s86, v0
	v_cmp_gt_i32_e64 s[48:49], s87, v98
	s_waitcnt lgkmcnt(0)
	v_max_f32_e32 v3, v3, v3
	v_max_f32_e32 v2, v2, v3
	ds_bpermute_b32 v3, v185, v2
	s_waitcnt lgkmcnt(0)
	v_max_f32_e32 v3, v3, v3
	v_max_f32_e32 v2, v2, v3
	ds_bpermute_b32 v3, v186, v2
	s_waitcnt lgkmcnt(0)
	v_max_f32_e32 v3, v3, v3
	v_max_f32_e32 v2, v2, v3
	ds_bpermute_b32 v3, v187, v2
	s_waitcnt lgkmcnt(0)
	v_max_f32_e32 v3, v3, v3
	v_max_f32_e32 v2, v2, v3
	ds_bpermute_b32 v3, v188, v2
	s_waitcnt lgkmcnt(0)
	v_max_f32_e32 v3, v3, v3
	v_max_f32_e32 v101, v2, v3
	ds_bpermute_b32 v102, v189, v101
	v_lshlrev_b64 v[2:3], 10, v[0:1]
	v_lshl_add_u64 v[206:207], v[2:3], 2, v[44:45]
	global_load_dwordx4 v[208:211], v[206:207], off offset:48
	global_load_dwordx4 v[212:215], v[206:207], off offset:32
	global_load_dwordx4 v[216:219], v[206:207], off offset:16
	global_load_dwordx4 v[220:223], v[206:207], off
	s_waitcnt lgkmcnt(0)
	v_max_f32_e32 v1, v102, v102
	v_max_f32_e32 v101, v101, v1
	v_div_scale_f32 v1, s[10:11], v101, v101, s12
	v_rcp_f32_e32 v102, v1
	v_div_scale_f32 v103, vcc, s12, v101, s12
	s_movk_i32 s10, 0x3fff
	v_fma_f32 v104, -v1, v102, 1.0
	v_fmac_f32_e32 v102, v104, v102
	v_mul_f32_e32 v104, v103, v102
	v_fma_f32 v105, -v1, v104, v103
	v_fmac_f32_e32 v104, v105, v102
	v_fma_f32 v1, -v1, v104, v103
	v_div_fmas_f32 v1, v1, v102, v104
	v_div_fixup_f32 v1, v1, v101, s12
	v_cmp_lt_f32_e32 vcc, 0, v101
	v_cmp_lt_i32_e64 s[50:51], s10, v98
	s_or_b64 s[8:9], s[50:51], s[8:9]
	v_cndmask_b32_e32 v102, 0, v1, vcc
	v_mul_f32_e32 v1, v6, v102
	v_mul_f32_e32 v6, v7, v102
	v_mul_f32_e32 v7, v8, v102
	v_mul_f32_e32 v8, v9, v102
	v_rndne_f32_e32 v1, v1
	v_rndne_f32_e32 v6, v6
	v_mul_f32_e32 v9, v10, v102
	v_mul_f32_e32 v10, v11, v102
	v_rndne_f32_e32 v7, v7
	v_rndne_f32_e32 v8, v8
	v_cvt_i32_f32_e32 v1, v1
	v_cvt_i32_f32_e32 v6, v6
	v_rndne_f32_e32 v9, v9
	v_rndne_f32_e32 v10, v10
	v_cvt_i32_f32_e32 v7, v7
	v_cvt_i32_f32_e32 v8, v8
	v_cvt_i32_f32_e32 v9, v9
	v_cvt_i32_f32_e32 v10, v10
	v_mul_f32_e32 v11, v12, v102
	v_add_u32_e32 v12, 8, v1
	v_add_u32_e32 v104, 8, v6
	v_and_b32_e32 v103, 15, v1
	v_lshlrev_b32_e32 v105, 4, v6
	v_add_u32_e32 v1, v1, v6
	v_lshl_add_u32 v6, v7, 4, v196
	v_lshl_add_u32 v107, v8, 8, v200
	v_lshrrev_b32_e32 v12, 4, v12
	v_and_b32_e32 v104, 0xf0, v104
	v_lshl_add_u32 v109, v9, 12, v201
	v_lshl_add_u32 v111, v10, 16, v202
	v_and_b32_e32 v6, 0xf00, v6
	v_and_b32_e32 v107, 0xf000, v107
	v_and_or_b32 v12, v12, 15, v104
	v_lshlrev_b32_e32 v106, 8, v7
	v_add3_u32 v1, v1, v7, v8
	v_and_b32_e32 v7, 0xf0000, v109
	v_and_b32_e32 v109, 0xf00000, v111
	v_or3_b32 v6, v12, v6, v107
	v_lshlrev_b32_e32 v110, 16, v9
	v_or3_b32 v6, v6, v7, v109
	v_add3_u32 v7, v1, v9, v10
	v_mul_f32_e32 v9, v13, v102
	v_rndne_f32_e32 v11, v11
	v_rndne_f32_e32 v9, v9
	v_cvt_i32_f32_e32 v11, v11
	v_cvt_i32_f32_e32 v9, v9
	v_lshlrev_b32_e32 v108, 12, v8
	v_and_b32_e32 v105, 0xf0, v105
	v_lshl_add_u32 v1, v11, 20, v203
	v_lshl_add_u32 v12, v9, 24, v204
	v_and_b32_e32 v1, 0xf000000, v1
	v_and_b32_e32 v12, 0xf0000000, v12
	v_and_b32_e32 v106, 0xf00, v106
	v_or3_b32 v1, v6, v1, v12
	v_lshl_or_b32 v6, v9, 28, v103
	v_lshlrev_b32_e32 v112, 20, v10
	v_and_b32_e32 v108, 0xf000, v108
	v_and_b32_e32 v8, 0xf0000, v110
	v_lshlrev_b32_e32 v10, 24, v11
	v_or3_b32 v6, v6, v105, v106
	v_and_b32_e32 v110, 0xf00000, v112
	v_and_b32_e32 v10, 0xf000000, v10
	v_or3_b32 v6, v6, v108, v8
	v_or3_b32 v10, v6, v110, v10
	v_add3_u32 v6, v7, v11, v9
	v_mul_f32_e32 v7, v14, v102
	v_mul_f32_e32 v8, v15, v102
	v_rndne_f32_e32 v7, v7
	v_rndne_f32_e32 v8, v8
	v_cvt_i32_f32_e32 v7, v7
	v_cvt_i32_f32_e32 v8, v8
	v_mul_f32_e32 v14, v99, v102
	v_mul_f32_e32 v15, v100, v102
	v_add_u32_e32 v9, 8, v7
	v_add_u32_e32 v11, 8, v8
	v_lshrrev_b32_e32 v9, 4, v9
	v_and_b32_e32 v11, 0xf0, v11
	v_and_or_b32 v9, v9, 15, v11
	v_mul_f32_e32 v11, v94, v102
	v_lshlrev_b32_e32 v13, 4, v8
	v_add3_u32 v6, v6, v7, v8
	v_mul_f32_e32 v8, v95, v102
	v_rndne_f32_e32 v11, v11
	v_rndne_f32_e32 v8, v8
	v_cvt_i32_f32_e32 v11, v11
	v_cvt_i32_f32_e32 v8, v8
	v_rndne_f32_e32 v14, v14
	v_rndne_f32_e32 v15, v15
	v_mul_f32_e32 v4, v4, v102
	v_mul_f32_e32 v5, v5, v102
	v_cvt_i32_f32_e32 v14, v14
	v_cvt_i32_f32_e32 v15, v15
	v_rndne_f32_e32 v4, v4
	v_rndne_f32_e32 v5, v5
	v_cvt_i32_f32_e32 v4, v4
	v_cvt_i32_f32_e32 v5, v5
	v_add3_u32 v6, v6, v11, v8
	v_add3_u32 v6, v6, v14, v15
	v_and_b32_e32 v12, 15, v7
	v_add3_u32 v6, v6, v4, v5
	v_cvt_f32_i32_e32 v6, v6
	v_lshl_add_u32 v7, v11, 4, v196
	v_lshlrev_b32_e32 v11, 8, v11
	v_and_b32_e32 v94, 0xf00, v11
	ds_bpermute_b32 v95, v184, v6
	v_lshl_add_u32 v11, v8, 8, v200
	v_and_b32_e32 v7, 0xf00, v7
	v_and_b32_e32 v11, 0xf000, v11
	v_or3_b32 v7, v9, v7, v11
	s_waitcnt lgkmcnt(0)
	v_add_f32_e32 v6, v95, v6
	ds_bpermute_b32 v9, v185, v6
	v_lshl_add_u32 v11, v14, 12, v201
	v_lshl_add_u32 v95, v15, 16, v202
	v_and_b32_e32 v11, 0xf0000, v11
	v_and_b32_e32 v95, 0xf00000, v95
	s_waitcnt lgkmcnt(0)
	v_add_f32_e32 v6, v6, v9
	ds_bpermute_b32 v9, v186, v6
	v_or3_b32 v7, v7, v11, v95
	v_lshlrev_b32_e32 v11, 20, v15
	v_and_b32_e32 v15, 0xf00000, v11
	v_lshl_add_u32 v11, v4, 20, v203
	s_waitcnt lgkmcnt(0)
	v_add_f32_e32 v6, v6, v9
	ds_bpermute_b32 v9, v187, v6
	v_lshl_add_u32 v95, v5, 24, v204
	v_and_b32_e32 v11, 0xf000000, v11
	v_and_b32_e32 v95, 0xf0000000, v95
	v_or3_b32 v11, v7, v11, v95
	s_waitcnt lgkmcnt(0)
	v_add_f32_e32 v6, v6, v9
	ds_bpermute_b32 v9, v188, v6
	v_and_b32_e32 v13, 0xf0, v13
	v_lshlrev_b32_e32 v8, 12, v8
	v_lshlrev_b32_e32 v14, 16, v14
	v_lshl_or_b32 v5, v5, 28, v12
	s_waitcnt lgkmcnt(0)
	v_add_f32_e32 v6, v6, v9
	ds_bpermute_b32 v7, v189, v6
	v_and_b32_e32 v8, 0xf000, v8
	v_and_b32_e32 v14, 0xf0000, v14
	v_lshlrev_b32_e32 v4, 24, v4
	v_or3_b32 v5, v5, v13, v94
	v_and_b32_e32 v4, 0xf000000, v4
	v_or3_b32 v5, v5, v8, v14
	v_or3_b32 v12, v5, v15, v4
	s_waitcnt lgkmcnt(0)
	v_add_f32_e32 v4, v6, v7
	v_mul_f32_e32 v13, 0x3c09ae41, v101
	v_mul_f32_e32 v14, 0.5, v4
	v_mov_b32_e32 v105, 0
	v_mov_b64_e32 v[4:5], v[48:49]
	v_mov_b32_e32 v104, 0
	v_mov_b32_e32 v103, 0
	v_mov_b32_e32 v102, 0
	v_mov_b32_e32 v101, 0
	v_mov_b32_e32 v100, 0
	v_mov_b32_e32 v99, 0
	v_mov_b32_e32 v15, 0
.LBB0_770:
	s_cmpk_eq_i32 s56, 0x80
	s_cselect_b64 s[10:11], -1, 0
	ds_bpermute_b32 v6, v97, v96
	s_and_b64 vcc, s[10:11], s[48:49]
	v_cndmask_b32_e32 v94, v0, v98, vcc
	v_ashrrev_i32_e32 v95, 31, v94
	s_and_b32 s10, s56, 0x70
	v_lshlrev_b64 v[94:95], 9, v[94:95]
	v_lshl_add_u64 v[94:95], s[94:95], 0, v[94:95]
	s_lshl_b32 s36, s10, 2
	s_waitcnt lgkmcnt(0)
	v_ashrrev_i32_e32 v7, 31, v6
	v_lshl_add_u64 v[94:95], v[94:95], 0, s[36:37]
	v_lshl_add_u64 v[6:7], v[6:7], 3, s[88:89]
	v_lshl_add_u64 v[94:95], v[94:95], 0, v[144:145]
	global_load_dwordx2 v[6:7], v[6:7], off
	s_nop 0
	global_load_dword v8, v[4:5], off
	global_load_dword v96, v[94:95], off
	s_waitcnt vmcnt(33)
	v_dot8_i32_i4 v9, v20, v1, 0
	v_dot8_i32_i4 v94, v20, v10, 0
	v_dot8_i32_i4 v9, v21, v11, v9
	v_dot8_i32_i4 v94, v21, v12, v94
	v_dot8_i32_i4 v20, v22, v1, 0
	v_dot8_i32_i4 v21, v22, v10, 0
	v_dot8_i32_i4 v20, v23, v11, v20
	v_dot8_i32_i4 v21, v23, v12, v21
	v_lshl_add_u32 v9, v9, 4, v94
	v_cvt_f32_i32_e32 v9, v9
	s_add_i32 s56, s56, 16
	v_lshl_add_u32 v20, v20, 4, v21
	v_cvt_f32_i32_e32 v94, v20
	s_waitcnt vmcnt(32)
	v_dot8_i32_i4 v20, v24, v1, 0
	v_dot8_i32_i4 v21, v24, v10, 0
	v_dot8_i32_i4 v20, v25, v11, v20
	v_dot8_i32_i4 v21, v25, v12, v21
	v_lshl_add_u64 v[4:5], v[4:5], 0, 64
	s_waitcnt vmcnt(2)
	v_mul_f32_e32 v7, v13, v7
	v_lshl_add_u32 v20, v20, 4, v21
	v_cvt_f32_i32_e32 v95, v20
	v_dot8_i32_i4 v20, v26, v1, 0
	v_dot8_i32_i4 v21, v26, v10, 0
	v_dot8_i32_i4 v20, v27, v11, v20
	v_dot8_i32_i4 v21, v27, v12, v21
	s_waitcnt vmcnt(0)
	v_readlane_b32 s10, v96, 0
	s_ashr_i32 s11, s10, 31
	v_readlane_b32 s12, v96, 1
	v_lshl_add_u32 v20, v20, 4, v21
	v_cvt_f32_i32_e32 v106, v20
	v_dot8_i32_i4 v20, v28, v1, 0
	v_dot8_i32_i4 v21, v28, v10, 0
	v_dot8_i32_i4 v20, v29, v11, v20
	v_dot8_i32_i4 v21, v29, v12, v21
	s_lshl_b64 s[10:11], s[10:11], 9
	s_ashr_i32 s13, s12, 31
	v_readlane_b32 s14, v96, 2
	v_lshl_add_u32 v20, v20, 4, v21
	v_cvt_f32_i32_e32 v107, v20
	v_dot8_i32_i4 v20, v30, v1, 0
	v_dot8_i32_i4 v21, v30, v10, 0
	v_dot8_i32_i4 v20, v31, v11, v20
	v_dot8_i32_i4 v21, v31, v12, v21
	s_lshl_b64 s[12:13], s[12:13], 9
	s_ashr_i32 s15, s14, 31
	v_readlane_b32 s16, v96, 3
	v_lshl_add_u32 v20, v20, 4, v21
	v_cvt_f32_i32_e32 v108, v20
	v_dot8_i32_i4 v20, v32, v1, 0
	v_dot8_i32_i4 v21, v32, v10, 0
	v_dot8_i32_i4 v20, v33, v11, v20
	v_dot8_i32_i4 v21, v33, v12, v21
	v_lshl_add_u64 v[22:23], v[16:17], 0, s[12:13]
	s_lshl_b64 s[14:15], s[14:15], 9
	s_ashr_i32 s17, s16, 31
	v_lshl_add_u32 v20, v20, 4, v21
	v_cvt_f32_i32_e32 v109, v20
	v_dot8_i32_i4 v20, v34, v1, 0
	v_dot8_i32_i4 v21, v34, v10, 0
	v_dot8_i32_i4 v20, v35, v11, v20
	v_dot8_i32_i4 v21, v35, v12, v21
	v_readlane_b32 s18, v96, 4
	global_load_dwordx2 v[22:23], v[22:23], off
	v_lshl_add_u64 v[24:25], v[16:17], 0, s[14:15]
	v_lshl_add_u32 v20, v20, 4, v21
	v_cvt_f32_i32_e32 v110, v20
	v_dot8_i32_i4 v20, v36, v1, 0
	v_dot8_i32_i4 v21, v36, v10, 0
	v_dot8_i32_i4 v20, v37, v11, v20
	v_dot8_i32_i4 v21, v37, v12, v21
	s_lshl_b64 s[16:17], s[16:17], 9
	s_ashr_i32 s19, s18, 31
	v_readlane_b32 s20, v96, 5
	v_lshl_add_u32 v20, v20, 4, v21
	v_cvt_f32_i32_e32 v111, v20
	v_dot8_i32_i4 v20, v38, v1, 0
	v_dot8_i32_i4 v21, v38, v10, 0
	v_dot8_i32_i4 v20, v39, v11, v20
	v_dot8_i32_i4 v21, v39, v12, v21
	v_cndmask_b32_e64 v119, v9, v111, s[40:41]
	v_cndmask_b32_e64 v9, v111, v9, s[40:41]
	ds_bpermute_b32 v111, v184, v119
	v_lshl_add_u32 v20, v20, 4, v21
	v_cvt_f32_i32_e32 v112, v20
	v_dot8_i32_i4 v20, v40, v1, 0
	v_dot8_i32_i4 v21, v40, v10, 0
	v_dot8_i32_i4 v20, v41, v11, v20
	v_dot8_i32_i4 v21, v41, v12, v21
	s_waitcnt lgkmcnt(0)
	v_add_f32_e32 v9, v9, v111
	v_cndmask_b32_e64 v111, v94, v112, s[40:41]
	ds_bpermute_b32 v111, v184, v111
	v_lshl_add_u32 v20, v20, 4, v21
	v_cvt_f32_i32_e32 v113, v20
	v_dot8_i32_i4 v20, v60, v1, 0
	v_dot8_i32_i4 v21, v60, v10, 0
	v_cndmask_b32_e64 v94, v112, v94, s[40:41]
	v_dot8_i32_i4 v20, v61, v11, v20
	v_dot8_i32_i4 v21, v61, v12, v21
	s_waitcnt lgkmcnt(0)
	v_add_f32_e32 v94, v94, v111
	v_cndmask_b32_e64 v111, v95, v113, s[40:41]
	ds_bpermute_b32 v111, v184, v111
	v_lshl_add_u32 v20, v20, 4, v21
	v_cvt_f32_i32_e32 v114, v20
	v_dot8_i32_i4 v20, v58, v1, 0
	v_dot8_i32_i4 v21, v58, v10, 0
	v_cndmask_b32_e64 v95, v113, v95, s[40:41]
	v_dot8_i32_i4 v20, v59, v11, v20
	v_dot8_i32_i4 v21, v59, v12, v21
	s_waitcnt lgkmcnt(0)
	v_add_f32_e32 v95, v95, v111
	v_cndmask_b32_e64 v111, v106, v114, s[40:41]
	ds_bpermute_b32 v111, v184, v111
	v_lshl_add_u32 v20, v20, 4, v21
	v_cvt_f32_i32_e32 v115, v20
	v_dot8_i32_i4 v20, v56, v1, 0
	v_dot8_i32_i4 v21, v56, v10, 0
	v_cndmask_b32_e64 v106, v114, v106, s[40:41]
	v_dot8_i32_i4 v20, v57, v11, v20
	v_dot8_i32_i4 v21, v57, v12, v21
	s_waitcnt lgkmcnt(0)
	v_add_f32_e32 v106, v106, v111
	v_cndmask_b32_e64 v111, v107, v115, s[40:41]
	ds_bpermute_b32 v111, v184, v111
	v_lshl_add_u32 v20, v20, 4, v21
	v_cvt_f32_i32_e32 v116, v20
	v_dot8_i32_i4 v20, v54, v1, 0
	v_dot8_i32_i4 v21, v54, v10, 0
	v_cndmask_b32_e64 v107, v115, v107, s[40:41]
	v_dot8_i32_i4 v20, v55, v11, v20
	v_dot8_i32_i4 v21, v55, v12, v21
	s_waitcnt lgkmcnt(0)
	v_add_f32_e32 v107, v107, v111
	v_cndmask_b32_e64 v111, v108, v116, s[40:41]
	ds_bpermute_b32 v111, v184, v111
	v_lshl_add_u32 v20, v20, 4, v21
	v_cvt_f32_i32_e32 v117, v20
	v_dot8_i32_i4 v20, v52, v1, 0
	v_dot8_i32_i4 v21, v52, v10, 0
	v_cndmask_b32_e64 v108, v116, v108, s[40:41]
	v_dot8_i32_i4 v20, v53, v11, v20
	v_dot8_i32_i4 v21, v53, v12, v21
	s_waitcnt lgkmcnt(0)
	v_add_f32_e32 v108, v108, v111
	v_cndmask_b32_e64 v111, v109, v117, s[40:41]
	ds_bpermute_b32 v111, v184, v111
	v_lshl_add_u32 v20, v20, 4, v21
	v_cvt_f32_i32_e32 v118, v20
	v_cndmask_b32_e64 v109, v117, v109, s[40:41]
	v_lshl_add_u64 v[20:21], v[16:17], 0, s[10:11]
	s_waitcnt lgkmcnt(0)
	v_add_f32_e32 v109, v109, v111
	v_cndmask_b32_e64 v111, v110, v118, s[40:41]
	ds_bpermute_b32 v111, v184, v111
	v_cndmask_b32_e64 v110, v118, v110, s[40:41]
	global_load_dwordx2 v[20:21], v[20:21], off
	v_lshl_add_u64 v[26:27], v[16:17], 0, s[16:17]
	global_load_dwordx2 v[24:25], v[24:25], off
	s_waitcnt lgkmcnt(0)
	v_add_f32_e32 v110, v110, v111
	v_cndmask_b32_e64 v111, v9, v107, s[42:43]
	v_cndmask_b32_e64 v9, v107, v9, s[42:43]
	ds_bpermute_b32 v107, v185, v111
	s_lshl_b64 s[18:19], s[18:19], 9
	s_ashr_i32 s21, s20, 31
	v_readlane_b32 s22, v96, 6
	global_load_dwordx2 v[26:27], v[26:27], off
	s_waitcnt lgkmcnt(0)
	v_add_f32_e32 v9, v9, v107
	v_cndmask_b32_e64 v107, v94, v108, s[42:43]
	ds_bpermute_b32 v107, v185, v107
	v_cndmask_b32_e64 v94, v108, v94, s[42:43]
	v_lshl_add_u64 v[28:29], v[16:17], 0, s[18:19]
	s_lshl_b64 s[20:21], s[20:21], 9
	s_ashr_i32 s23, s22, 31
	s_waitcnt lgkmcnt(0)
	v_add_f32_e32 v94, v94, v107
	v_cndmask_b32_e64 v107, v95, v109, s[42:43]
	ds_bpermute_b32 v107, v185, v107
	v_cndmask_b32_e64 v95, v109, v95, s[42:43]
	v_readlane_b32 s24, v96, 7
	global_load_dwordx2 v[28:29], v[28:29], off
	v_lshl_add_u64 v[30:31], v[16:17], 0, s[20:21]
	s_waitcnt lgkmcnt(0)
	v_add_f32_e32 v95, v95, v107
	v_cndmask_b32_e64 v107, v106, v110, s[42:43]
	ds_bpermute_b32 v107, v185, v107
	v_cndmask_b32_e64 v106, v110, v106, s[42:43]
	s_lshl_b64 s[22:23], s[22:23], 9
	s_ashr_i32 s25, s24, 31
	v_readlane_b32 s26, v96, 8
	s_waitcnt lgkmcnt(0)
	v_add_f32_e32 v106, v106, v107
	v_cndmask_b32_e64 v107, v9, v95, s[44:45]
	v_cndmask_b32_e64 v9, v95, v9, s[44:45]
	ds_bpermute_b32 v95, v186, v107
	global_load_dwordx2 v[30:31], v[30:31], off
	v_lshl_add_u64 v[32:33], v[16:17], 0, s[22:23]
	s_lshl_b64 s[24:25], s[24:25], 9
	s_ashr_i32 s27, s26, 31
	s_waitcnt lgkmcnt(0)
	v_add_f32_e32 v9, v9, v95
	v_cndmask_b32_e64 v95, v94, v106, s[44:45]
	ds_bpermute_b32 v95, v186, v95
	v_cndmask_b32_e64 v94, v106, v94, s[44:45]
	v_readlane_b32 s28, v96, 9
	global_load_dwordx2 v[32:33], v[32:33], off
	v_lshl_add_u64 v[34:35], v[16:17], 0, s[24:25]
	s_waitcnt lgkmcnt(0)
	v_add_f32_e32 v94, v94, v95
	v_cndmask_b32_e64 v95, v9, v94, s[46:47]
	v_cndmask_b32_e64 v9, v94, v9, s[46:47]
	ds_bpermute_b32 v94, v187, v95
	s_lshl_b64 s[26:27], s[26:27], 9
	s_ashr_i32 s29, s28, 31
	v_readlane_b32 s30, v96, 10
	global_load_dwordx2 v[34:35], v[34:35], off
	s_waitcnt lgkmcnt(0)
	v_add_f32_e32 v9, v9, v94
	ds_bpermute_b32 v94, v188, v9
	v_lshl_add_u64 v[36:37], v[16:17], 0, s[26:27]
	s_lshl_b64 s[28:29], s[28:29], 9
	s_ashr_i32 s31, s30, 31
	v_readlane_b32 s34, v96, 11
	s_waitcnt lgkmcnt(0)
	v_add_f32_e32 v9, v9, v94
	ds_bpermute_b32 v94, v189, v9
	global_load_dwordx2 v[36:37], v[36:37], off
	v_lshl_add_u64 v[38:39], v[16:17], 0, s[28:29]
	s_lshl_b64 s[30:31], s[30:31], 9
	s_ashr_i32 s35, s34, 31
	s_waitcnt lgkmcnt(0)
	v_add_f32_e32 v9, v9, v94
	v_add_f32_e32 v9, v14, v9
	v_mul_f32_e32 v7, v7, v9
	v_mul_f32_e32 v9, 0x3d372713, v7
	v_mul_f32_e32 v9, v7, v9
	v_fma_f32 v9, v7, v9, v7
	v_mul_f32_e32 v9, 0x3fcc422a, v9
	v_mul_f32_e32 v9, 0xbfb8aa3b, v9
	v_exp_f32_e32 v9, v9
	v_lshlrev_b32_e32 v94, 4, v92
	v_readlane_b32 s38, v96, 12
	global_load_dwordx2 v[38:39], v[38:39], off
	v_add_f32_e32 v9, 1.0, v9
	v_rcp_f32_e32 v9, v9
	v_lshl_add_u64 v[40:41], v[16:17], 0, s[30:31]
	s_lshl_b64 s[34:35], s[34:35], 9
	s_ashr_i32 s39, s38, 31
	v_pk_mul_f32 v[6:7], v[6:7], v[8:9]
	v_lshrrev_b32_e32 v9, 4, v92
	v_pk_mul_f32 v[6:7], v[6:7], v[6:7] op_sel:[0,1] op_sel_hi:[1,0]
	v_cvt_f16_f32_e32 v120, v6
	v_and_b32_e32 v8, 0x7070707, v92
	v_readlane_b32 s36, v120, 0
	v_and_b32_e32 v9, 0x7070707, v9
	v_perm_b32 v8, s2, v205, v8
	v_perm_b32 v9, s2, v205, v9
	v_and_or_b32 v8, v94, s4, v8
	v_and_or_b32 v9, v92, s4, v9
	v_perm_b32 v92, v9, v8, s5
	v_perm_b32 v94, v9, v8, s33
	v_perm_b32 v95, v9, v8, s0
	v_perm_b32 v8, v9, v8, s1
	v_pk_fma_f16 v8, v8, s36, v102 op_sel_hi:[1,0,1]
	v_lshrrev_b32_e32 v102, 4, v93
	v_pk_fma_f16 v9, v92, s36, v105 op_sel_hi:[1,0,1]
	v_pk_fma_f16 v92, v94, s36, v104 op_sel_hi:[1,0,1]
	v_pk_fma_f16 v94, v95, s36, v103 op_sel_hi:[1,0,1]
	v_and_b32_e32 v95, 0x7070707, v93
	v_and_b32_e32 v102, 0x7070707, v102
	v_perm_b32 v95, s2, v205, v95
	v_perm_b32 v102, s2, v205, v102
	v_lshlrev_b32_e32 v103, 4, v93
	v_and_or_b32 v95, v103, s4, v95
	v_and_or_b32 v93, v93, s4, v102
	v_perm_b32 v102, v93, v95, s5
	v_perm_b32 v103, v93, v95, s33
	v_perm_b32 v104, v93, v95, s0
	v_perm_b32 v93, v93, v95, s1
	v_pk_fma_f16 v95, v102, s36, v101 op_sel_hi:[1,0,1]
	v_readlane_b32 s59, v120, 4
	v_lshrrev_b32_e32 v101, 4, v90
	v_pk_fma_f16 v100, v103, s36, v100 op_sel_hi:[1,0,1]
	v_pk_fma_f16 v99, v104, s36, v99 op_sel_hi:[1,0,1]
	v_pk_fma_f16 v7, v93, s36, v15 op_sel_hi:[1,0,1]
	v_and_b32_e32 v93, 0x7070707, v90
	v_and_b32_e32 v101, 0x7070707, v101
	v_perm_b32 v93, s2, v205, v93
	v_perm_b32 v101, s2, v205, v101
	v_lshlrev_b32_e32 v102, 4, v90
	v_and_or_b32 v93, v102, s4, v93
	v_and_or_b32 v90, v90, s4, v101
	v_perm_b32 v103, v90, v93, s0
	v_perm_b32 v101, v90, v93, s5
	v_perm_b32 v102, v90, v93, s33
	v_perm_b32 v90, v90, v93, s1
	v_pk_fma_f16 v93, v103, s59, v94 op_sel_hi:[1,0,1]
	v_lshrrev_b32_e32 v94, 4, v91
	v_pk_fma_f16 v8, v90, s59, v8 op_sel_hi:[1,0,1]
	v_and_b32_e32 v90, 0x7070707, v91
	v_and_b32_e32 v94, 0x7070707, v94
	v_pk_fma_f16 v9, v101, s59, v9 op_sel_hi:[1,0,1]
	v_perm_b32 v90, s2, v205, v90
	v_perm_b32 v94, s2, v205, v94
	v_lshlrev_b32_e32 v101, 4, v91
	v_and_or_b32 v90, v101, s4, v90
	v_and_or_b32 v91, v91, s4, v94
	v_pk_fma_f16 v92, v102, s59, v92 op_sel_hi:[1,0,1]
	v_perm_b32 v94, v91, v90, s5
	v_perm_b32 v102, v91, v90, s0
	v_perm_b32 v101, v91, v90, s33
	v_perm_b32 v90, v91, v90, s1
	v_pk_fma_f16 v91, v94, s59, v95 op_sel_hi:[1,0,1]
	v_pk_fma_f16 v95, v102, s59, v99 op_sel_hi:[1,0,1]
	v_readlane_b32 s60, v120, 8
	v_lshrrev_b32_e32 v99, 4, v88
	v_pk_fma_f16 v94, v101, s59, v100 op_sel_hi:[1,0,1]
	v_pk_fma_f16 v7, v90, s59, v7 op_sel_hi:[1,0,1]
	v_and_b32_e32 v90, 0x7070707, v88
	v_and_b32_e32 v99, 0x7070707, v99
	v_perm_b32 v90, s2, v205, v90
	v_perm_b32 v99, s2, v205, v99
	v_lshlrev_b32_e32 v100, 4, v88
	v_and_or_b32 v90, v100, s4, v90
	v_and_or_b32 v88, v88, s4, v99
	v_perm_b32 v100, v88, v90, s33
	v_perm_b32 v101, v88, v90, s0
	v_perm_b32 v99, v88, v90, s5
	v_perm_b32 v88, v88, v90, s1
	v_pk_fma_f16 v90, v100, s60, v92 op_sel_hi:[1,0,1]
	v_pk_fma_f16 v92, v101, s60, v93 op_sel_hi:[1,0,1]
	v_lshrrev_b32_e32 v93, 4, v89
	v_pk_fma_f16 v8, v88, s60, v8 op_sel_hi:[1,0,1]
	v_and_b32_e32 v88, 0x7070707, v89
	v_and_b32_e32 v93, 0x7070707, v93
	v_pk_fma_f16 v9, v99, s60, v9 op_sel_hi:[1,0,1]
	v_perm_b32 v88, s2, v205, v88
	v_perm_b32 v93, s2, v205, v93
	v_lshlrev_b32_e32 v99, 4, v89
	v_and_or_b32 v88, v99, s4, v88
	v_and_or_b32 v89, v89, s4, v93
	v_perm_b32 v93, v89, v88, s5
	v_perm_b32 v99, v89, v88, s33
	v_perm_b32 v100, v89, v88, s0
	v_perm_b32 v88, v89, v88, s1
	v_pk_fma_f16 v89, v93, s60, v91 op_sel_hi:[1,0,1]
	v_pk_fma_f16 v91, v99, s60, v94 op_sel_hi:[1,0,1]
	v_readlane_b32 s36, v120, 12
	v_lshrrev_b32_e32 v94, 4, v86
	v_pk_fma_f16 v93, v100, s60, v95 op_sel_hi:[1,0,1]
	v_pk_fma_f16 v7, v88, s60, v7 op_sel_hi:[1,0,1]
	v_and_b32_e32 v88, 0x7070707, v86
	v_and_b32_e32 v94, 0x7070707, v94
	v_perm_b32 v88, s2, v205, v88
	v_perm_b32 v94, s2, v205, v94
	v_lshlrev_b32_e32 v95, 4, v86
	v_and_or_b32 v88, v95, s4, v88
	v_and_or_b32 v86, v86, s4, v94
	v_perm_b32 v95, v86, v88, s33
	v_perm_b32 v99, v86, v88, s0
	v_perm_b32 v94, v86, v88, s5
	v_perm_b32 v86, v86, v88, s1
	v_pk_fma_f16 v88, v95, s36, v90 op_sel_hi:[1,0,1]
	v_pk_fma_f16 v90, v99, s36, v92 op_sel_hi:[1,0,1]
	v_lshrrev_b32_e32 v92, 4, v87
	v_pk_fma_f16 v8, v86, s36, v8 op_sel_hi:[1,0,1]
	v_and_b32_e32 v86, 0x7070707, v87
	v_and_b32_e32 v92, 0x7070707, v92
	v_pk_fma_f16 v9, v94, s36, v9 op_sel_hi:[1,0,1]
	v_perm_b32 v86, s2, v205, v86
	v_perm_b32 v92, s2, v205, v92
	v_lshlrev_b32_e32 v94, 4, v87
	v_and_or_b32 v86, v94, s4, v86
	v_and_or_b32 v87, v87, s4, v92
	v_perm_b32 v92, v87, v86, s5
	v_perm_b32 v94, v87, v86, s33
	v_perm_b32 v95, v87, v86, s0
	v_perm_b32 v86, v87, v86, s1
	v_pk_fma_f16 v87, v92, s36, v89 op_sel_hi:[1,0,1]
	v_readlane_b32 s59, v120, 16
	v_lshrrev_b32_e32 v92, 4, v84
	v_pk_fma_f16 v89, v94, s36, v91 op_sel_hi:[1,0,1]
	v_pk_fma_f16 v91, v95, s36, v93 op_sel_hi:[1,0,1]
	v_pk_fma_f16 v7, v86, s36, v7 op_sel_hi:[1,0,1]
	v_and_b32_e32 v86, 0x7070707, v84
	v_and_b32_e32 v92, 0x7070707, v92
	v_perm_b32 v86, s2, v205, v86
	v_perm_b32 v92, s2, v205, v92
	v_lshlrev_b32_e32 v93, 4, v84
	v_and_or_b32 v86, v93, s4, v86
	v_and_or_b32 v84, v84, s4, v92
	v_perm_b32 v93, v84, v86, s33
	v_perm_b32 v94, v84, v86, s0
	v_perm_b32 v92, v84, v86, s5
	v_perm_b32 v84, v84, v86, s1
	v_pk_fma_f16 v86, v93, s59, v88 op_sel_hi:[1,0,1]
	v_pk_fma_f16 v88, v94, s59, v90 op_sel_hi:[1,0,1]
	v_lshrrev_b32_e32 v90, 4, v85
	v_pk_fma_f16 v8, v84, s59, v8 op_sel_hi:[1,0,1]
	v_and_b32_e32 v84, 0x7070707, v85
	v_and_b32_e32 v90, 0x7070707, v90
	v_pk_fma_f16 v9, v92, s59, v9 op_sel_hi:[1,0,1]
	v_perm_b32 v84, s2, v205, v84
	v_perm_b32 v90, s2, v205, v90
	v_lshlrev_b32_e32 v92, 4, v85
	v_and_or_b32 v84, v92, s4, v84
	v_and_or_b32 v85, v85, s4, v90
	v_perm_b32 v90, v85, v84, s5
	v_perm_b32 v92, v85, v84, s33
	v_perm_b32 v93, v85, v84, s0
	v_perm_b32 v84, v85, v84, s1
	v_pk_fma_f16 v85, v90, s59, v87 op_sel_hi:[1,0,1]
	v_readlane_b32 s60, v120, 20
	v_lshrrev_b32_e32 v90, 4, v82
	v_pk_fma_f16 v87, v92, s59, v89 op_sel_hi:[1,0,1]
	v_pk_fma_f16 v89, v93, s59, v91 op_sel_hi:[1,0,1]
	v_pk_fma_f16 v7, v84, s59, v7 op_sel_hi:[1,0,1]
	v_and_b32_e32 v84, 0x7070707, v82
	v_and_b32_e32 v90, 0x7070707, v90
	v_perm_b32 v84, s2, v205, v84
	v_perm_b32 v90, s2, v205, v90
	v_lshlrev_b32_e32 v91, 4, v82
	v_and_or_b32 v84, v91, s4, v84
	v_and_or_b32 v82, v82, s4, v90
	v_perm_b32 v91, v82, v84, s33
	v_perm_b32 v92, v82, v84, s0
	v_perm_b32 v90, v82, v84, s5
	v_perm_b32 v82, v82, v84, s1
	v_pk_fma_f16 v84, v91, s60, v86 op_sel_hi:[1,0,1]
	v_pk_fma_f16 v86, v92, s60, v88 op_sel_hi:[1,0,1]
	v_lshrrev_b32_e32 v88, 4, v83
	v_pk_fma_f16 v8, v82, s60, v8 op_sel_hi:[1,0,1]
	v_and_b32_e32 v82, 0x7070707, v83
	v_and_b32_e32 v88, 0x7070707, v88
	v_pk_fma_f16 v9, v90, s60, v9 op_sel_hi:[1,0,1]
	v_perm_b32 v82, s2, v205, v82
	v_perm_b32 v88, s2, v205, v88
	v_lshlrev_b32_e32 v90, 4, v83
	v_and_or_b32 v82, v90, s4, v82
	v_and_or_b32 v83, v83, s4, v88
	v_perm_b32 v88, v83, v82, s5
	v_perm_b32 v90, v83, v82, s33
	v_perm_b32 v91, v83, v82, s0
	v_perm_b32 v82, v83, v82, s1
	v_pk_fma_f16 v83, v88, s60, v85 op_sel_hi:[1,0,1]
	v_readlane_b32 s36, v120, 24
	v_lshrrev_b32_e32 v88, 4, v80
	v_pk_fma_f16 v85, v90, s60, v87 op_sel_hi:[1,0,1]
	v_pk_fma_f16 v87, v91, s60, v89 op_sel_hi:[1,0,1]
	v_pk_fma_f16 v7, v82, s60, v7 op_sel_hi:[1,0,1]
	v_and_b32_e32 v82, 0x7070707, v80
	v_and_b32_e32 v88, 0x7070707, v88
	v_perm_b32 v82, s2, v205, v82
	v_perm_b32 v88, s2, v205, v88
	v_lshlrev_b32_e32 v89, 4, v80
	v_and_or_b32 v82, v89, s4, v82
	v_and_or_b32 v80, v80, s4, v88
	v_perm_b32 v89, v80, v82, s33
	v_perm_b32 v90, v80, v82, s0
	v_perm_b32 v88, v80, v82, s5
	v_perm_b32 v80, v80, v82, s1
	v_pk_fma_f16 v82, v89, s36, v84 op_sel_hi:[1,0,1]
	v_pk_fma_f16 v84, v90, s36, v86 op_sel_hi:[1,0,1]
	v_lshrrev_b32_e32 v86, 4, v81
	v_pk_fma_f16 v8, v80, s36, v8 op_sel_hi:[1,0,1]
	v_and_b32_e32 v80, 0x7070707, v81
	v_and_b32_e32 v86, 0x7070707, v86
	v_pk_fma_f16 v9, v88, s36, v9 op_sel_hi:[1,0,1]
	v_perm_b32 v80, s2, v205, v80
	v_perm_b32 v86, s2, v205, v86
	v_lshlrev_b32_e32 v88, 4, v81
	v_and_or_b32 v80, v88, s4, v80
	v_and_or_b32 v81, v81, s4, v86
	v_perm_b32 v86, v81, v80, s5
	v_perm_b32 v88, v81, v80, s33
	v_perm_b32 v89, v81, v80, s0
	v_perm_b32 v80, v81, v80, s1
	v_pk_fma_f16 v81, v86, s36, v83 op_sel_hi:[1,0,1]
	v_readlane_b32 s59, v120, 28
	v_lshrrev_b32_e32 v86, 4, v78
	v_pk_fma_f16 v83, v88, s36, v85 op_sel_hi:[1,0,1]
	v_pk_fma_f16 v85, v89, s36, v87 op_sel_hi:[1,0,1]
	v_pk_fma_f16 v7, v80, s36, v7 op_sel_hi:[1,0,1]
	v_and_b32_e32 v80, 0x7070707, v78
	v_and_b32_e32 v86, 0x7070707, v86
	v_perm_b32 v80, s2, v205, v80
	v_perm_b32 v86, s2, v205, v86
	v_lshlrev_b32_e32 v87, 4, v78
	v_and_or_b32 v80, v87, s4, v80
	v_and_or_b32 v78, v78, s4, v86
	v_perm_b32 v87, v78, v80, s33
	v_perm_b32 v88, v78, v80, s0
	v_perm_b32 v86, v78, v80, s5
	v_perm_b32 v78, v78, v80, s1
	v_pk_fma_f16 v80, v87, s59, v82 op_sel_hi:[1,0,1]
	v_pk_fma_f16 v82, v88, s59, v84 op_sel_hi:[1,0,1]
	v_lshrrev_b32_e32 v84, 4, v79
	v_pk_fma_f16 v8, v78, s59, v8 op_sel_hi:[1,0,1]
	v_and_b32_e32 v78, 0x7070707, v79
	v_and_b32_e32 v84, 0x7070707, v84
	v_pk_fma_f16 v9, v86, s59, v9 op_sel_hi:[1,0,1]
	v_perm_b32 v78, s2, v205, v78
	v_perm_b32 v84, s2, v205, v84
	v_lshlrev_b32_e32 v86, 4, v79
	v_and_or_b32 v78, v86, s4, v78
	v_and_or_b32 v79, v79, s4, v84
	v_perm_b32 v84, v79, v78, s5
	v_perm_b32 v86, v79, v78, s33
	v_perm_b32 v87, v79, v78, s0
	v_perm_b32 v78, v79, v78, s1
	v_pk_fma_f16 v79, v84, s59, v81 op_sel_hi:[1,0,1]
	v_readlane_b32 s60, v120, 32
	v_lshrrev_b32_e32 v84, 4, v76
	v_pk_fma_f16 v81, v86, s59, v83 op_sel_hi:[1,0,1]
	v_pk_fma_f16 v83, v87, s59, v85 op_sel_hi:[1,0,1]
	v_pk_fma_f16 v7, v78, s59, v7 op_sel_hi:[1,0,1]
	v_and_b32_e32 v78, 0x7070707, v76
	v_and_b32_e32 v84, 0x7070707, v84
	v_perm_b32 v78, s2, v205, v78
	v_perm_b32 v84, s2, v205, v84
	v_lshlrev_b32_e32 v85, 4, v76
	v_and_or_b32 v78, v85, s4, v78
	v_and_or_b32 v76, v76, s4, v84
	v_perm_b32 v85, v76, v78, s33
	v_perm_b32 v86, v76, v78, s0
	v_perm_b32 v84, v76, v78, s5
	v_perm_b32 v76, v76, v78, s1
	v_pk_fma_f16 v78, v85, s60, v80 op_sel_hi:[1,0,1]
	v_pk_fma_f16 v80, v86, s60, v82 op_sel_hi:[1,0,1]
	v_lshrrev_b32_e32 v82, 4, v77
	v_pk_fma_f16 v8, v76, s60, v8 op_sel_hi:[1,0,1]
	v_and_b32_e32 v76, 0x7070707, v77
	v_and_b32_e32 v82, 0x7070707, v82
	v_pk_fma_f16 v9, v84, s60, v9 op_sel_hi:[1,0,1]
	v_perm_b32 v76, s2, v205, v76
	v_perm_b32 v82, s2, v205, v82
	v_lshlrev_b32_e32 v84, 4, v77
	v_and_or_b32 v76, v84, s4, v76
	v_and_or_b32 v77, v77, s4, v82
	v_perm_b32 v82, v77, v76, s5
	v_perm_b32 v84, v77, v76, s33
	v_perm_b32 v85, v77, v76, s0
	v_perm_b32 v76, v77, v76, s1
	v_pk_fma_f16 v77, v82, s60, v79 op_sel_hi:[1,0,1]
	v_readlane_b32 s36, v120, 36
	v_lshrrev_b32_e32 v82, 4, v70
	v_pk_fma_f16 v79, v84, s60, v81 op_sel_hi:[1,0,1]
	v_pk_fma_f16 v81, v85, s60, v83 op_sel_hi:[1,0,1]
	v_pk_fma_f16 v7, v76, s60, v7 op_sel_hi:[1,0,1]
	v_and_b32_e32 v76, 0x7070707, v70
	v_and_b32_e32 v82, 0x7070707, v82
	v_perm_b32 v76, s2, v205, v76
	v_perm_b32 v82, s2, v205, v82
	v_lshlrev_b32_e32 v83, 4, v70
	v_and_or_b32 v76, v83, s4, v76
	v_and_or_b32 v70, v70, s4, v82
	v_perm_b32 v83, v70, v76, s33
	v_perm_b32 v84, v70, v76, s0
	v_perm_b32 v82, v70, v76, s5
	v_perm_b32 v70, v70, v76, s1
	v_pk_fma_f16 v76, v83, s36, v78 op_sel_hi:[1,0,1]
	v_pk_fma_f16 v78, v84, s36, v80 op_sel_hi:[1,0,1]
	v_lshrrev_b32_e32 v80, 4, v71
	v_pk_fma_f16 v8, v70, s36, v8 op_sel_hi:[1,0,1]
	v_and_b32_e32 v70, 0x7070707, v71
	v_and_b32_e32 v80, 0x7070707, v80
	v_pk_fma_f16 v9, v82, s36, v9 op_sel_hi:[1,0,1]
	v_perm_b32 v70, s2, v205, v70
	v_perm_b32 v80, s2, v205, v80
	v_lshlrev_b32_e32 v82, 4, v71
	v_and_or_b32 v70, v82, s4, v70
	v_and_or_b32 v71, v71, s4, v80
	v_perm_b32 v80, v71, v70, s5
	v_perm_b32 v82, v71, v70, s33
	v_perm_b32 v83, v71, v70, s0
	v_perm_b32 v70, v71, v70, s1
	v_pk_fma_f16 v71, v80, s36, v77 op_sel_hi:[1,0,1]
	v_readlane_b32 s59, v120, 40
	v_lshrrev_b32_e32 v80, 4, v66
	v_pk_fma_f16 v77, v82, s36, v79 op_sel_hi:[1,0,1]
	v_pk_fma_f16 v79, v83, s36, v81 op_sel_hi:[1,0,1]
	v_pk_fma_f16 v7, v70, s36, v7 op_sel_hi:[1,0,1]
	v_and_b32_e32 v70, 0x7070707, v66
	v_and_b32_e32 v80, 0x7070707, v80
	v_perm_b32 v70, s2, v205, v70
	v_perm_b32 v80, s2, v205, v80
	v_lshlrev_b32_e32 v81, 4, v66
	v_and_or_b32 v70, v81, s4, v70
	v_and_or_b32 v66, v66, s4, v80
	v_perm_b32 v81, v66, v70, s33
	v_perm_b32 v82, v66, v70, s0
	v_perm_b32 v80, v66, v70, s5
	v_perm_b32 v66, v66, v70, s1
	v_pk_fma_f16 v70, v81, s59, v76 op_sel_hi:[1,0,1]
	v_pk_fma_f16 v76, v82, s59, v78 op_sel_hi:[1,0,1]
	v_lshrrev_b32_e32 v78, 4, v67
	v_pk_fma_f16 v8, v66, s59, v8 op_sel_hi:[1,0,1]
	v_and_b32_e32 v66, 0x7070707, v67
	v_and_b32_e32 v78, 0x7070707, v78
	v_pk_fma_f16 v9, v80, s59, v9 op_sel_hi:[1,0,1]
	v_perm_b32 v66, s2, v205, v66
	v_perm_b32 v78, s2, v205, v78
	v_lshlrev_b32_e32 v80, 4, v67
	v_and_or_b32 v66, v80, s4, v66
	v_and_or_b32 v67, v67, s4, v78
	v_perm_b32 v78, v67, v66, s5
	v_perm_b32 v80, v67, v66, s33
	v_perm_b32 v81, v67, v66, s0
	v_perm_b32 v66, v67, v66, s1
	v_pk_fma_f16 v67, v78, s59, v71 op_sel_hi:[1,0,1]
	v_readlane_b32 s60, v120, 44
	v_lshrrev_b32_e32 v78, 4, v72
	v_pk_fma_f16 v71, v80, s59, v77 op_sel_hi:[1,0,1]
	v_pk_fma_f16 v77, v81, s59, v79 op_sel_hi:[1,0,1]
	v_pk_fma_f16 v7, v66, s59, v7 op_sel_hi:[1,0,1]
	v_and_b32_e32 v66, 0x7070707, v72
	v_and_b32_e32 v78, 0x7070707, v78
	v_perm_b32 v66, s2, v205, v66
	v_perm_b32 v78, s2, v205, v78
	v_lshlrev_b32_e32 v79, 4, v72
	v_and_or_b32 v66, v79, s4, v66
	v_and_or_b32 v72, v72, s4, v78
	v_perm_b32 v80, v72, v66, s0
	v_perm_b32 v78, v72, v66, s5
	v_perm_b32 v79, v72, v66, s33
	v_perm_b32 v66, v72, v66, s1
	v_pk_fma_f16 v72, v80, s60, v76 op_sel_hi:[1,0,1]
	v_lshrrev_b32_e32 v76, 4, v73
	v_pk_fma_f16 v8, v66, s60, v8 op_sel_hi:[1,0,1]
	v_and_b32_e32 v66, 0x7070707, v73
	v_and_b32_e32 v76, 0x7070707, v76
	v_pk_fma_f16 v9, v78, s60, v9 op_sel_hi:[1,0,1]
	v_perm_b32 v66, s2, v205, v66
	v_perm_b32 v76, s2, v205, v76
	v_lshlrev_b32_e32 v78, 4, v73
	v_and_or_b32 v66, v78, s4, v66
	v_and_or_b32 v73, v73, s4, v76
	v_perm_b32 v76, v73, v66, s5
	v_pk_fma_f16 v70, v79, s60, v70 op_sel_hi:[1,0,1]
	v_perm_b32 v78, v73, v66, s33
	v_perm_b32 v79, v73, v66, s0
	v_perm_b32 v66, v73, v66, s1
	v_pk_fma_f16 v67, v76, s60, v67 op_sel_hi:[1,0,1]
	v_readlane_b32 s36, v120, 48
	v_lshrrev_b32_e32 v76, 4, v68
	v_pk_fma_f16 v71, v78, s60, v71 op_sel_hi:[1,0,1]
	v_pk_fma_f16 v73, v79, s60, v77 op_sel_hi:[1,0,1]
	v_pk_fma_f16 v7, v66, s60, v7 op_sel_hi:[1,0,1]
	v_and_b32_e32 v66, 0x7070707, v68
	v_and_b32_e32 v76, 0x7070707, v76
	v_perm_b32 v66, s2, v205, v66
	v_perm_b32 v76, s2, v205, v76
	v_lshlrev_b32_e32 v77, 4, v68
	v_and_or_b32 v66, v77, s4, v66
	v_and_or_b32 v68, v68, s4, v76
	v_perm_b32 v77, v68, v66, s33
	v_perm_b32 v78, v68, v66, s0
	v_perm_b32 v76, v68, v66, s5
	v_perm_b32 v66, v68, v66, s1
	v_pk_fma_f16 v68, v77, s36, v70 op_sel_hi:[1,0,1]
	v_pk_fma_f16 v70, v78, s36, v72 op_sel_hi:[1,0,1]
	v_lshrrev_b32_e32 v72, 4, v69
	v_pk_fma_f16 v8, v66, s36, v8 op_sel_hi:[1,0,1]
	v_and_b32_e32 v66, 0x7070707, v69
	v_and_b32_e32 v72, 0x7070707, v72
	v_pk_fma_f16 v9, v76, s36, v9 op_sel_hi:[1,0,1]
	v_perm_b32 v66, s2, v205, v66
	v_perm_b32 v72, s2, v205, v72
	v_lshlrev_b32_e32 v76, 4, v69
	v_and_or_b32 v66, v76, s4, v66
	v_and_or_b32 v69, v69, s4, v72
	v_perm_b32 v72, v69, v66, s5
	v_perm_b32 v76, v69, v66, s33
	v_perm_b32 v77, v69, v66, s0
	v_perm_b32 v66, v69, v66, s1
	v_pk_fma_f16 v67, v72, s36, v67 op_sel_hi:[1,0,1]
	v_readlane_b32 s59, v120, 52
	v_lshrrev_b32_e32 v72, 4, v64
	v_pk_fma_f16 v69, v76, s36, v71 op_sel_hi:[1,0,1]
	v_pk_fma_f16 v71, v77, s36, v73 op_sel_hi:[1,0,1]
	v_pk_fma_f16 v7, v66, s36, v7 op_sel_hi:[1,0,1]
	v_and_b32_e32 v66, 0x7070707, v64
	v_and_b32_e32 v72, 0x7070707, v72
	v_perm_b32 v66, s2, v205, v66
	v_perm_b32 v72, s2, v205, v72
	v_lshlrev_b32_e32 v73, 4, v64
	v_and_or_b32 v66, v73, s4, v66
	v_and_or_b32 v64, v64, s4, v72
	v_perm_b32 v73, v64, v66, s33
	v_perm_b32 v76, v64, v66, s0
	v_perm_b32 v72, v64, v66, s5
	v_perm_b32 v64, v64, v66, s1
	v_pk_fma_f16 v66, v73, s59, v68 op_sel_hi:[1,0,1]
	v_pk_fma_f16 v68, v76, s59, v70 op_sel_hi:[1,0,1]
	v_lshrrev_b32_e32 v70, 4, v65
	v_pk_fma_f16 v8, v64, s59, v8 op_sel_hi:[1,0,1]
	v_and_b32_e32 v64, 0x7070707, v65
	v_and_b32_e32 v70, 0x7070707, v70
	v_pk_fma_f16 v9, v72, s59, v9 op_sel_hi:[1,0,1]
	v_perm_b32 v64, s2, v205, v64
	v_perm_b32 v70, s2, v205, v70
	v_lshlrev_b32_e32 v72, 4, v65
	v_and_or_b32 v64, v72, s4, v64
	v_and_or_b32 v65, v65, s4, v70
	v_perm_b32 v70, v65, v64, s5
	v_perm_b32 v72, v65, v64, s33
	v_perm_b32 v73, v65, v64, s0
	v_perm_b32 v64, v65, v64, s1
	v_pk_fma_f16 v65, v70, s59, v67 op_sel_hi:[1,0,1]
	v_readlane_b32 s60, v120, 56
	v_lshrrev_b32_e32 v70, 4, v62
	v_pk_fma_f16 v67, v72, s59, v69 op_sel_hi:[1,0,1]
	v_pk_fma_f16 v69, v73, s59, v71 op_sel_hi:[1,0,1]
	v_pk_fma_f16 v7, v64, s59, v7 op_sel_hi:[1,0,1]
	v_and_b32_e32 v64, 0x7070707, v62
	v_and_b32_e32 v70, 0x7070707, v70
	v_perm_b32 v64, s2, v205, v64
	v_perm_b32 v70, s2, v205, v70
	v_lshlrev_b32_e32 v71, 4, v62
	v_and_or_b32 v64, v71, s4, v64
	v_and_or_b32 v62, v62, s4, v70
	v_perm_b32 v71, v62, v64, s33
	v_perm_b32 v72, v62, v64, s0
	v_perm_b32 v70, v62, v64, s5
	v_perm_b32 v62, v62, v64, s1
	v_pk_fma_f16 v64, v71, s60, v66 op_sel_hi:[1,0,1]
	v_pk_fma_f16 v66, v72, s60, v68 op_sel_hi:[1,0,1]
	v_lshrrev_b32_e32 v68, 4, v63
	v_pk_fma_f16 v8, v62, s60, v8 op_sel_hi:[1,0,1]
	v_and_b32_e32 v62, 0x7070707, v63
	v_and_b32_e32 v68, 0x7070707, v68
	v_pk_fma_f16 v9, v70, s60, v9 op_sel_hi:[1,0,1]
	v_perm_b32 v62, s2, v205, v62
	v_perm_b32 v68, s2, v205, v68
	v_lshlrev_b32_e32 v70, 4, v63
	v_and_or_b32 v62, v70, s4, v62
	v_and_or_b32 v63, v63, s4, v68
	v_perm_b32 v68, v63, v62, s5
	v_perm_b32 v70, v63, v62, s33
	v_perm_b32 v71, v63, v62, s0
	v_perm_b32 v62, v63, v62, s1
	v_pk_fma_f16 v7, v62, s60, v7 op_sel_hi:[1,0,1]
	v_readlane_b32 s36, v120, 60
	v_lshrrev_b32_e32 v62, 4, v50
	v_pk_fma_f16 v63, v68, s60, v65 op_sel_hi:[1,0,1]
	v_pk_fma_f16 v65, v70, s60, v67 op_sel_hi:[1,0,1]
	v_pk_fma_f16 v67, v71, s60, v69 op_sel_hi:[1,0,1]
	v_and_b32_e32 v15, 0x7070707, v50
	v_and_b32_e32 v62, 0x7070707, v62
	v_perm_b32 v15, s2, v205, v15
	v_perm_b32 v62, s2, v205, v62
	v_lshlrev_b32_e32 v68, 4, v50
	v_and_or_b32 v15, v68, s4, v15
	v_and_or_b32 v50, v50, s4, v62
	v_perm_b32 v62, v50, v15, s5
	v_perm_b32 v68, v50, v15, s33
	v_perm_b32 v69, v50, v15, s0
	v_perm_b32 v15, v50, v15, s1
	v_pk_fma_f16 v105, v62, s36, v9 op_sel_hi:[1,0,1]
	v_lshrrev_b32_e32 v9, 4, v51
	v_pk_fma_f16 v102, v15, s36, v8 op_sel_hi:[1,0,1]
	v_and_b32_e32 v8, 0x7070707, v51
	v_and_b32_e32 v9, 0x7070707, v9
	v_perm_b32 v8, s2, v205, v8
	v_perm_b32 v9, s2, v205, v9
	v_lshlrev_b32_e32 v15, 4, v51
	v_and_or_b32 v8, v15, s4, v8
	v_and_or_b32 v9, v51, s4, v9
	v_perm_b32 v15, v9, v8, s5
	v_perm_b32 v50, v9, v8, s33
	v_perm_b32 v51, v9, v8, s0
	v_perm_b32 v8, v9, v8, s1
	v_pk_fma_f16 v104, v68, s36, v64 op_sel_hi:[1,0,1]
	v_pk_fma_f16 v103, v69, s36, v66 op_sel_hi:[1,0,1]
	v_pk_fma_f16 v101, v15, s36, v63 op_sel_hi:[1,0,1]
	v_pk_fma_f16 v100, v50, s36, v65 op_sel_hi:[1,0,1]
	v_pk_fma_f16 v99, v51, s36, v67 op_sel_hi:[1,0,1]
	v_pk_fma_f16 v15, v8, s36, v7 op_sel_hi:[1,0,1]
	v_lshl_add_u64 v[6:7], v[18:19], 0, s[10:11]
	global_load_dwordx2 v[92:93], v[6:7], off
	v_lshl_add_u64 v[6:7], v[18:19], 0, s[12:13]
	global_load_dwordx2 v[90:91], v[6:7], off
	v_lshl_add_u64 v[6:7], v[18:19], 0, s[14:15]
	global_load_dwordx2 v[88:89], v[6:7], off
	v_lshl_add_u64 v[6:7], v[18:19], 0, s[16:17]
	global_load_dwordx2 v[86:87], v[6:7], off
	v_lshl_add_u64 v[6:7], v[18:19], 0, s[18:19]
	global_load_dwordx2 v[84:85], v[6:7], off
	v_lshl_add_u64 v[6:7], v[18:19], 0, s[20:21]
	global_load_dwordx2 v[82:83], v[6:7], off
	v_lshl_add_u64 v[6:7], v[18:19], 0, s[22:23]
	global_load_dwordx2 v[80:81], v[6:7], off
	v_lshl_add_u64 v[6:7], v[18:19], 0, s[24:25]
	global_load_dwordx2 v[78:79], v[6:7], off
	v_lshl_add_u64 v[6:7], v[18:19], 0, s[26:27]
	global_load_dwordx2 v[76:77], v[6:7], off
	v_lshl_add_u64 v[6:7], v[18:19], 0, s[28:29]
	v_readlane_b32 s50, v96, 13
	global_load_dwordx2 v[70:71], v[6:7], off
	v_lshl_add_u64 v[6:7], v[18:19], 0, s[30:31]
	global_load_dwordx2 v[40:41], v[40:41], off
	v_lshl_add_u64 v[52:53], v[16:17], 0, s[34:35]
	s_lshl_b64 s[38:39], s[38:39], 9
	s_ashr_i32 s51, s50, 31
	v_readlane_b32 s52, v96, 14
	global_load_dwordx2 v[66:67], v[6:7], off
	v_lshl_add_u64 v[6:7], v[18:19], 0, s[34:35]
	global_load_dwordx2 v[60:61], v[52:53], off
	global_load_dwordx2 v[72:73], v[6:7], off
	v_lshl_add_u64 v[52:53], v[16:17], 0, s[38:39]
	s_lshl_b64 s[50:51], s[50:51], 9
	s_ashr_i32 s53, s52, 31
	v_readlane_b32 s54, v96, 15
	v_lshl_add_u64 v[6:7], v[18:19], 0, s[38:39]
	global_load_dwordx2 v[58:59], v[52:53], off
	global_load_dwordx2 v[68:69], v[6:7], off
	v_lshl_add_u64 v[52:53], v[16:17], 0, s[50:51]
	s_lshl_b64 s[52:53], s[52:53], 9
	s_ashr_i32 s55, s54, 31
	v_lshl_add_u64 v[6:7], v[18:19], 0, s[50:51]
	global_load_dwordx2 v[56:57], v[52:53], off
	global_load_dwordx2 v[64:65], v[6:7], off
	v_lshl_add_u64 v[52:53], v[16:17], 0, s[52:53]
	s_lshl_b64 s[54:55], s[54:55], 9
	v_lshl_add_u64 v[6:7], v[18:19], 0, s[52:53]
	global_load_dwordx2 v[54:55], v[52:53], off
	global_load_dwordx2 v[62:63], v[6:7], off
	v_lshl_add_u64 v[52:53], v[16:17], 0, s[54:55]
	v_lshl_add_u64 v[6:7], v[18:19], 0, s[54:55]
	global_load_dwordx2 v[52:53], v[52:53], off
	s_cmpk_eq_i32 s56, 0x90
	global_load_dwordx2 v[50:51], v[6:7], off
	s_cbranch_scc0 .LBB0_770
	v_lshl_add_u64 v[94:95], v[2:3], 2, v[44:45]
	v_mov_b32_e32 v106, v208
	v_mov_b32_e32 v107, v209
	v_mov_b32_e32 v108, v210
	v_mov_b32_e32 v109, v211
	v_mov_b32_e32 v8, v212
	v_mov_b32_e32 v9, v213
	v_mov_b32_e32 v10, v214
	v_mov_b32_e32 v11, v215
	v_mov_b32_e32 v4, v216
	v_mov_b32_e32 v5, v217
	v_mov_b32_e32 v6, v218
	v_mov_b32_e32 v7, v219
	v_mov_b32_e32 v0, v220
	v_mov_b32_e32 v1, v221
	v_mov_b32_e32 v2, v222
	v_mov_b32_e32 v3, v223
	v_cvt_f32_f16_sdwa v13, v105 dst_sel:DWORD dst_unused:UNUSED_PAD src0_sel:WORD_1
	v_cvt_f32_f16_e32 v12, v105
	s_mov_b32 s12, 0x800000
	v_readlane_b32 s10, v255, 5
	v_readlane_b32 s11, v255, 6
	v_pk_add_f32 v[0:1], v[0:1], v[12:13]
	v_cvt_f32_f16_sdwa v13, v104 dst_sel:DWORD dst_unused:UNUSED_PAD src0_sel:WORD_1
	v_cvt_f32_f16_e32 v12, v104
	v_lshl_add_u64 v[48:49], v[48:49], 0, s[10:11]
	v_pk_add_f32 v[2:3], v[2:3], v[12:13]
	v_cvt_f32_f16_sdwa v13, v103 dst_sel:DWORD dst_unused:UNUSED_PAD src0_sel:WORD_1
	v_cvt_f32_f16_e32 v12, v103
	global_store_dwordx4 v[94:95], v[0:3], off
	v_pk_add_f32 v[4:5], v[4:5], v[12:13]
	v_cvt_f32_f16_sdwa v13, v102 dst_sel:DWORD dst_unused:UNUSED_PAD src0_sel:WORD_1
	v_cvt_f32_f16_e32 v12, v102
	v_mov_b32_e32 v102, v1
	v_mov_b32_e32 v103, v5
	v_pk_mul_f32 v[102:103], v[102:103], v[102:103]
	v_pk_add_f32 v[6:7], v[6:7], v[12:13]
	v_mov_b32_e32 v12, v0
	v_mov_b32_e32 v13, v4
	v_pk_fma_f32 v[12:13], v[12:13], v[12:13], v[102:103]
	v_mov_b32_e32 v102, v2
	v_mov_b32_e32 v103, v6
	v_pk_fma_f32 v[12:13], v[102:103], v[102:103], v[12:13]
	v_mov_b32_e32 v102, v3
	v_mov_b32_e32 v103, v7
	v_pk_fma_f32 v[102:103], v[102:103], v[102:103], v[12:13]
	v_cvt_f32_f16_sdwa v13, v101 dst_sel:DWORD dst_unused:UNUSED_PAD src0_sel:WORD_1
	v_cvt_f32_f16_e32 v12, v101
	v_cvt_f32_f16_sdwa v101, v15 dst_sel:DWORD dst_unused:UNUSED_PAD src0_sel:WORD_1
	global_store_dwordx4 v[94:95], v[4:7], off offset:16
	v_pk_add_f32 v[8:9], v[8:9], v[12:13]
	v_cvt_f32_f16_sdwa v13, v100 dst_sel:DWORD dst_unused:UNUSED_PAD src0_sel:WORD_1
	v_cvt_f32_f16_e32 v12, v100
	v_cvt_f32_f16_e32 v100, v15
	v_pk_add_f32 v[10:11], v[10:11], v[12:13]
	v_cvt_f32_f16_sdwa v13, v99 dst_sel:DWORD dst_unused:UNUSED_PAD src0_sel:WORD_1
	v_cvt_f32_f16_e32 v12, v99
	v_pk_add_f32 v[14:15], v[108:109], v[100:101]
	v_mov_b32_e32 v100, v9
	global_store_dwordx4 v[94:95], v[8:11], off offset:32
	v_pk_add_f32 v[12:13], v[106:107], v[12:13]
	global_store_dwordx4 v[94:95], v[12:15], off offset:48
	v_mov_b32_e32 v101, v13
	v_mov_b32_e32 v94, v8
	v_mov_b32_e32 v95, v12
	v_pk_mul_f32 v[100:101], v[100:101], v[100:101]
	v_add_f32_e32 v99, v102, v103
	v_pk_fma_f32 v[94:95], v[94:95], v[94:95], v[100:101]
	v_mov_b32_e32 v100, v10
	v_mov_b32_e32 v101, v14
	v_pk_fma_f32 v[94:95], v[100:101], v[100:101], v[94:95]
	v_mov_b32_e32 v100, v11
	v_mov_b32_e32 v101, v15
	v_pk_fma_f32 v[94:95], v[100:101], v[100:101], v[94:95]
	global_load_dwordx4 v[100:103], v[46:47], off offset:48
	global_load_dwordx4 v[104:107], v[46:47], off offset:32
	global_load_dwordx4 v[108:111], v[46:47], off offset:16
	global_load_dwordx4 v[112:115], v[46:47], off
	v_add_f32_e32 v94, v99, v94
	v_add_f32_e32 v94, v94, v95
	ds_bpermute_b32 v95, v184, v94
	s_waitcnt lgkmcnt(0)
	v_add_f32_e32 v94, v94, v95
	ds_bpermute_b32 v95, v185, v94
	s_waitcnt lgkmcnt(0)
	v_add_f32_e32 v94, v94, v95
	ds_bpermute_b32 v95, v186, v94
	s_waitcnt lgkmcnt(0)
	v_add_f32_e32 v94, v94, v95
	ds_bpermute_b32 v95, v187, v94
	s_waitcnt lgkmcnt(0)
	v_add_f32_e32 v94, v94, v95
	ds_bpermute_b32 v95, v188, v94
	s_waitcnt lgkmcnt(0)
	v_add_f32_e32 v94, v94, v95
	ds_bpermute_b32 v95, v189, v94
	s_waitcnt lgkmcnt(0)
	v_add_f32_e32 v94, v94, v95
	v_fmamk_f32 v94, v94, 0x3a800000, v191
	v_cmp_gt_f32_e32 vcc, s12, v94
	v_mul_f32_e32 v95, 0x4b800000, v94
	s_nop 0
	v_cndmask_b32_e32 v94, v94, v95, vcc
	v_rsq_f32_e32 v94, v94
	s_nop 0
	v_mul_f32_e32 v95, 0x45800000, v94
	v_cndmask_b32_e32 v94, v94, v95, vcc
	v_pk_mul_f32 v[0:1], v[0:1], v[94:95] op_sel_hi:[1,0]
	v_pk_mul_f32 v[2:3], v[2:3], v[94:95] op_sel_hi:[1,0]
	s_waitcnt vmcnt(0)
	v_pk_mul_f32 v[0:1], v[112:113], v[0:1]
	v_pk_mul_f32 v[2:3], v[114:115], v[2:3]
	v_cvt_pk_bf16_f32 v0, v0, v1
	v_cvt_pk_bf16_f32 v1, v2, v3
	v_pk_mul_f32 v[2:3], v[4:5], v[94:95] op_sel_hi:[1,0]
	v_pk_mul_f32 v[4:5], v[6:7], v[94:95] op_sel_hi:[1,0]
	v_pk_mul_f32 v[2:3], v[108:109], v[2:3]
	v_pk_mul_f32 v[4:5], v[110:111], v[4:5]
	v_cvt_pk_bf16_f32 v2, v2, v3
	v_cvt_pk_bf16_f32 v3, v4, v5
	v_pk_mul_f32 v[4:5], v[8:9], v[94:95] op_sel_hi:[1,0]
	v_pk_mul_f32 v[6:7], v[10:11], v[94:95] op_sel_hi:[1,0]
	v_pk_mul_f32 v[4:5], v[104:105], v[4:5]
	v_pk_mul_f32 v[6:7], v[6:7], v[106:107]
	v_cvt_pk_bf16_f32 v4, v4, v5
	v_cvt_pk_bf16_f32 v5, v6, v7
	v_pk_mul_f32 v[6:7], v[12:13], v[94:95] op_sel_hi:[1,0]
	v_pk_mul_f32 v[8:9], v[14:15], v[94:95] op_sel_hi:[1,0]
	v_pk_mul_f32 v[6:7], v[6:7], v[100:101]
	v_pk_mul_f32 v[8:9], v[8:9], v[102:103]
	v_cvt_pk_bf16_f32 v6, v6, v7
	v_cvt_pk_bf16_f32 v7, v8, v9
	global_store_dwordx4 v[74:75], v[0:3], off
	global_store_dwordx4 v[74:75], v[4:7], off offset:16
	s_nop 0
	v_mov_b32_e32 v0, v98
	s_andn2_b64 exec, exec, s[8:9]
	s_cbranch_execnz .LBB0_769
